# baseline (speedup 1.0000x reference)
_Z16closed_form_mainPKfS0_PKiPf:
	s_load_dwordx8 s[16:23], s[0:1], 0x0
	s_lshr_b32 s6, s2, 3
	v_readfirstlane_b32 s0, v0
	s_mul_hi_u32 s7, s6, 0x24924925
	s_lshr_b32 s4, s0, 6
	s_and_b32 s0, s2, 7
	s_mul_i32 s1, s7, 7
	s_bfe_u32 s5, s2, 0x10003
	s_sub_i32 s1, s6, s1
	s_mul_i32 s36, s0, 7
	s_xor_b32 s3, s4, s5
	s_add_i32 s36, s36, s1
	s_waitcnt lgkmcnt(0)
	s_mov_b64 s[28:29], s[22:23]
	v_and_b32_e32 v19, 63, v0
	s_cmp_lt_u32 s36, 52
	s_mov_b64 s[0:1], -1
	s_cbranch_scc0 .LBB0_32
	s_mul_hi_u32 s0, s6, 0x20820821
	s_lshr_b32 s38, s0, 3
	s_mul_hi_u32 s0, s7, 0x1c71c71d
	s_mul_i32 s0, s0, 9
	s_sub_i32 s0, s7, s0
	v_add_u32_e32 v2, -3, v19
	v_mad_u64_u32 v[0:1], s[0:1], s0, 57, v[2:3]
	s_mov_b64 s[24:25], s[18:19]
	v_mov_b32_e32 v1, 0x200
	v_med3_i32 v1, v0, 0, v1
	s_mul_i32 s34, s36, 10
	s_and_b32 s17, s17, 0xffff
	s_and_b32 s25, s25, 0xffff
	v_cmp_gt_u32_e64 s[0:1], 57, v2
	s_mov_b32 s19, 0x20000
	s_mov_b32 s18, 0xe0e038
	s_mov_b32 s26, 0x606018
	s_mul_i32 s35, s38, 0x70701c
	s_mul_i32 s33, s38, 0x30300c
	v_lshlrev_b32_e32 v28, 2, v1
	v_mul_u32_u24_e32 v27, 12, v1
	v_lshlrev_b32_e32 v23, 4, v19
	s_cmp_lg_u32 s4, s5
	v_sub_u32_e64 v29, s34, 2 clamp
	s_cbranch_scc0 .LBB0_15
	s_setprio 2
	s_mov_b32 s27, s19
	s_and_b32 s21, s21, 0xffff
	s_mov_b32 s22, 0x202008
	s_mov_b32 s23, s19
	s_mul_i32 s38, s38, 0x101004
	s_movk_i32 s37, 0x80
	v_add_u32_e32 v18, -1, v0
	s_movk_i32 s4, 0x201
	s_movk_i32 s5, 0x1ff
	v_cmp_gt_u32_e64 s[40:41], s4, v0
	v_cmp_gt_u32_e64 s[42:43], s5, v18
	v_mov_b32_e32 v18, 0x42c80000
	v_mov_b32_e32 v22, 0x3de38e39
	v_mov_b32_e32 v26, 0x3a3d6628
	v_mov_b32_e32 v1, 0
	s_add_i32 s4, s34, -3
	s_max_i32 s4, s4, 0
	s_mul_i32 s4, s4, 0x804
	s_add_i32 s4, s4, s38
	buffer_load_dword v29, v28, s[20:23], s4 offen nt
	s_add_i32 s4, s34, -2
	s_max_i32 s4, s4, 0
	s_mul_i32 s4, s4, 0x804
	s_add_i32 s4, s4, s38
	buffer_load_dword v2, v28, s[20:23], s4 offen nt
	s_add_i32 s5, s34, -2
	s_max_i32 s5, s5, 0
	s_mul_i32 s6, s5, 0x804
	s_add_i32 s6, s6, s35
	s_add_i32 s7, s6, 0x505014
	s_add_i32 s8, s6, 0x606018
	s_mul_i32 s9, s5, 0x180c
	s_add_i32 s9, s9, s33
	s_add_i32 s4, s34, -1
	s_max_i32 s4, s4, 0
	s_mul_i32 s4, s4, 0x804
	s_add_i32 s4, s4, s38
	buffer_load_dword v3, v28, s[20:23], s4 offen nt
	buffer_load_dwordx3 v[8:10], v27, s[24:27], s9 offen nt
	buffer_load_dword v4, v28, s[16:19], s7 offen nt
	buffer_load_dword v5, v28, s[16:19], s8 offen nt
	s_add_i32 s5, s34, -1
	s_max_i32 s5, s5, 0
	s_mul_i32 s6, s5, 0x804
	s_add_i32 s6, s6, s35
	s_add_i32 s7, s6, 0x505014
	s_add_i32 s8, s6, 0x606018
	s_mul_i32 s9, s5, 0x180c
	s_add_i32 s9, s9, s33
	s_add_i32 s4, s34, 0
	s_min_i32 s4, s4, 0x200
	s_mul_i32 s4, s4, 0x804
	s_add_i32 s4, s4, s38
	buffer_load_dword v16, v28, s[20:23], s4 offen nt
	buffer_load_dwordx3 v[12:14], v27, s[24:27], s9 offen nt
	buffer_load_dword v6, v28, s[16:19], s7 offen nt
	buffer_load_dword v7, v28, s[16:19], s8 offen nt
	s_add_i32 s5, s34, 0
	s_min_i32 s5, s5, 0x200
	s_mul_i32 s6, s5, 0x804
	s_add_i32 s6, s6, s35
	s_add_i32 s7, s6, 0x505014
	s_add_i32 s8, s6, 0x606018
	s_mul_i32 s9, s5, 0x180c
	s_add_i32 s9, s9, s33
	s_add_i32 s4, s34, 1
	s_min_i32 s4, s4, 0x200
	s_mul_i32 s4, s4, 0x804
	s_add_i32 s4, s4, s38
	buffer_load_dword v17, v28, s[20:23], s4 offen nt
	buffer_load_dwordx3 v[32:34], v27, s[24:27], s9 offen nt
	buffer_load_dword v20, v28, s[16:19], s7 offen nt
	buffer_load_dword v21, v28, s[16:19], s8 offen nt
	s_waitcnt vmcnt(12)
	s_add_i32 s4, s34, -3
	s_cmpk_lt_u32 s4, 0x201
	s_cselect_b64 s[12:13], s[40:41], 0
	v_cmp_eq_u32_e64 s[14:15], s37, v29
	s_and_b64 s[14:15], s[14:15], s[12:13]
	v_cndmask_b32_e64 v24, 0, 1, s[14:15]
	s_add_i32 s4, s34, -2
	s_cmpk_lt_u32 s4, 0x201
	s_cselect_b64 s[12:13], s[40:41], 0
	v_cmp_eq_u32_e64 s[14:15], s37, v2
	s_and_b64 s[14:15], s[14:15], s[12:13]
	v_cndmask_b32_e64 v25, 0, 1, s[14:15]
	s_nop 0
	v_or_b32_dpp v30, v24, v24 wave_shr:1 row_mask:0xf bank_mask:0xf bound_ctrl:1
	v_or_b32_dpp v31, v25, v25 wave_shr:1 row_mask:0xf bank_mask:0xf bound_ctrl:1
	s_nop 1
	v_or_b32_dpp v30, v24, v30 wave_shl:1 row_mask:0xf bank_mask:0xf bound_ctrl:1
	v_or_b32_dpp v31, v25, v31 wave_shl:1 row_mask:0xf bank_mask:0xf bound_ctrl:1
	s_nop 1
	v_or_b32_dpp v36, v30, v30 wave_shr:1 row_mask:0xf bank_mask:0xf bound_ctrl:1
	v_or_b32_dpp v37, v31, v31 wave_shr:1 row_mask:0xf bank_mask:0xf bound_ctrl:1
	s_nop 1
	v_or_b32_dpp v36, v30, v36 wave_shl:1 row_mask:0xf bank_mask:0xf bound_ctrl:1
	v_or_b32_dpp v37, v31, v37 wave_shl:1 row_mask:0xf bank_mask:0xf bound_ctrl:1
	v_mov_b32_e32 v24, 0
	v_mov_b32_e32 v25, 0
	s_waitcnt vmcnt(8)
	v_mov_b32_dpp v40, v8 wave_shr:1 row_mask:0xf bank_mask:0xf bound_ctrl:1
	v_mov_b32_dpp v41, v9 wave_shr:1 row_mask:0xf bank_mask:0xf bound_ctrl:1
	v_mov_b32_dpp v42, v10 wave_shr:1 row_mask:0xf bank_mask:0xf bound_ctrl:1
	v_mov_b32_dpp v44, v8 wave_shl:1 row_mask:0xf bank_mask:0xf bound_ctrl:1
	v_mov_b32_dpp v45, v9 wave_shl:1 row_mask:0xf bank_mask:0xf bound_ctrl:1
	v_mov_b32_dpp v46, v10 wave_shl:1 row_mask:0xf bank_mask:0xf bound_ctrl:1
	s_add_i32 s4, s34, -1
	s_cmpk_lt_u32 s4, 0x201
	s_cselect_b64 s[12:13], s[40:41], 0
	v_cmp_eq_u32_e64 s[14:15], s37, v3
	s_and_b64 s[14:15], s[14:15], s[12:13]
	v_cndmask_b32_e64 v30, 0, 1, s[14:15]
	v_pk_add_f32 v[38:39], v[8:9], v[40:41]
	v_pk_mul_f32 v[48:49], v[8:9], v[8:9] op_sel_hi:[0,1]
	v_or_b32_dpp v31, v30, v30 wave_shr:1 row_mask:0xf bank_mask:0xf bound_ctrl:1
	v_pk_mul_f32 v[50:51], v[8:9], v[10:11] op_sel_hi:[1,0]
	v_or_b32_dpp v31, v30, v31 wave_shl:1 row_mask:0xf bank_mask:0xf bound_ctrl:1
	v_mul_f32_e64 v52, v9, v9
	v_mul_f32_e64 v53, v10, v10
	v_or_b32_dpp v56, v31, v31 wave_shr:1 row_mask:0xf bank_mask:0xf bound_ctrl:1
	v_add_f32_e64 v54, v10, v42
	v_pk_add_f32 v[38:39], v[38:39], v[44:45]
	v_or_b32_dpp v56, v31, v56 wave_shl:1 row_mask:0xf bank_mask:0xf bound_ctrl:1
	v_or3_b32 v57, v56, v37, v36
	v_or3_b32 v57, v57, v24, v25
	s_add_i32 s4, s34, -4
	s_cmpk_lt_u32 s4, 0x1ff
	s_cselect_b64 s[12:13], s[42:43], 0
	v_cmp_ne_u32_e64 s[30:31], 0, v57
	s_and_b64 s[30:31], s[30:31], s[12:13]
	v_cndmask_b32_e64 v57, 0, 1.0, s[30:31]
	v_pk_fma_f32 v[48:49], v[40:41], v[40:41], v[48:49] op_sel_hi:[0,1,1]
	v_pk_fma_f32 v[50:51], v[40:41], v[42:43], v[50:51] op_sel_hi:[1,0,1]
	v_fma_f32 v52, v41, v41, v52
	v_fma_f32 v53, v42, v42, v53
	v_add_f32_dpp v55, v57, v57 wave_shr:1 row_mask:0xf bank_mask:0xf bound_ctrl:1
	v_add_f32_e64 v54, v54, v46
	v_pk_fma_f32 v[48:49], v[44:45], v[44:45], v[48:49] op_sel_hi:[0,1,1]
	v_pk_fma_f32 v[50:51], v[44:45], v[46:47], v[50:51] op_sel_hi:[1,0,1]
	v_fma_f32 v52, v45, v45, v52
	v_fma_f32 v53, v46, v46, v53
	v_add_f32_dpp v55, v57, v55 wave_shl:1 row_mask:0xf bank_mask:0xf bound_ctrl:1
	v_mov_b32_dpp v30, v4 wave_shr:1 row_mask:0xf bank_mask:0xf bound_ctrl:1
	v_mov_b32_dpp v31, v5 wave_shr:1 row_mask:0xf bank_mask:0xf bound_ctrl:1
	v_mov_b32_dpp v58, v4 wave_shl:1 row_mask:0xf bank_mask:0xf bound_ctrl:1
	v_mov_b32_dpp v59, v5 wave_shl:1 row_mask:0xf bank_mask:0xf bound_ctrl:1
	v_pk_mul_f32 v[60:61], v[4:5], v[8:9] op_sel_hi:[1,0]
	v_pk_mul_f32 v[64:65], v[4:5], v[8:9] op_sel:[0,1]
	v_pk_mul_f32 v[68:69], v[4:5], v[10:11] op_sel_hi:[1,0]
	v_pk_add_f32 v[72:73], v[4:5], v[30:31]
	v_pk_fma_f32 v[60:61], v[30:31], v[40:41], v[60:61] op_sel_hi:[1,0,1]
	v_pk_fma_f32 v[64:65], v[30:31], v[40:41], v[64:65] op_sel:[0,1,0]
	v_pk_fma_f32 v[68:69], v[30:31], v[42:43], v[68:69] op_sel_hi:[1,0,1]
	v_pk_add_f32 v[72:73], v[72:73], v[58:59]
	v_pk_fma_f32 v[60:61], v[58:59], v[44:45], v[60:61] op_sel_hi:[1,0,1]
	v_pk_fma_f32 v[64:65], v[58:59], v[44:45], v[64:65] op_sel:[0,1,0]
	v_pk_fma_f32 v[68:69], v[58:59], v[46:47], v[68:69] op_sel_hi:[1,0,1]
	s_barrier
	s_add_i32 s5, s34, 1
	s_min_i32 s5, s5, 0x200
	s_mul_i32 s6, s5, 0x804
	s_add_i32 s6, s6, s35
	s_add_i32 s7, s6, 0x505014
	s_add_i32 s8, s6, 0x606018
	s_mul_i32 s9, s5, 0x180c
	s_add_i32 s9, s9, s33
	s_add_i32 s4, s34, 2
	s_min_i32 s4, s4, 0x200
	s_mul_i32 s4, s4, 0x804
	s_add_i32 s4, s4, s38
	buffer_load_dword v25, v28, s[20:23], s4 offen nt
	buffer_load_dwordx3 v[76:78], v27, s[24:27], s9 offen nt
	buffer_load_dword v30, v28, s[16:19], s7 offen nt
	buffer_load_dword v31, v28, s[16:19], s8 offen nt
	s_waitcnt vmcnt(8)
	s_add_i32 s4, s34, 0
	s_cmpk_lt_u32 s4, 0x201
	s_cselect_b64 s[12:13], s[40:41], 0
	v_cmp_eq_u32_e64 s[14:15], s37, v16
	s_and_b64 s[14:15], s[14:15], s[12:13]
	v_cndmask_b32_e64 v57, 0, 1, s[14:15]
	v_mov_b32_dpp v80, v12 wave_shr:1 row_mask:0xf bank_mask:0xf bound_ctrl:1
	v_mov_b32_dpp v81, v13 wave_shr:1 row_mask:0xf bank_mask:0xf bound_ctrl:1
	v_or_b32_dpp v58, v57, v57 wave_shr:1 row_mask:0xf bank_mask:0xf bound_ctrl:1
	v_mov_b32_dpp v82, v14 wave_shr:1 row_mask:0xf bank_mask:0xf bound_ctrl:1
	v_or_b32_dpp v58, v57, v58 wave_shl:1 row_mask:0xf bank_mask:0xf bound_ctrl:1
	v_mov_b32_dpp v84, v12 wave_shl:1 row_mask:0xf bank_mask:0xf bound_ctrl:1
	v_mov_b32_dpp v85, v13 wave_shl:1 row_mask:0xf bank_mask:0xf bound_ctrl:1
	v_or_b32_dpp v59, v58, v58 wave_shr:1 row_mask:0xf bank_mask:0xf bound_ctrl:1
	v_mov_b32_dpp v86, v14 wave_shl:1 row_mask:0xf bank_mask:0xf bound_ctrl:1
	v_or_b32_dpp v59, v58, v59 wave_shl:1 row_mask:0xf bank_mask:0xf bound_ctrl:1
	s_waitcnt vmcnt(8)
	v_pk_add_f32 v[62:63], v[12:13], v[80:81]
	v_pk_mul_f32 v[66:67], v[12:13], v[12:13] op_sel_hi:[0,1]
	v_pk_mul_f32 v[70:71], v[12:13], v[14:15] op_sel_hi:[1,0]
	v_mul_f32_e64 v74, v13, v13
	v_mul_f32_e64 v75, v14, v14
	v_add_f32_e64 v88, v14, v82
	v_pk_add_f32 v[62:63], v[62:63], v[84:85]
	v_or3_b32 v57, v59, v56, v37
	v_or3_b32 v57, v57, v36, v24
	s_add_i32 s4, s34, -3
	s_cmpk_lt_u32 s4, 0x1ff
	s_cselect_b64 s[12:13], s[42:43], 0
	v_cmp_ne_u32_e64 s[30:31], 0, v57
	s_and_b64 s[30:31], s[30:31], s[12:13]
	v_cndmask_b32_e64 v57, 0, 1.0, s[30:31]
	v_pk_fma_f32 v[66:67], v[80:81], v[80:81], v[66:67] op_sel_hi:[0,1,1]
	v_pk_fma_f32 v[70:71], v[80:81], v[82:83], v[70:71] op_sel_hi:[1,0,1]
	v_fma_f32 v74, v81, v81, v74
	v_fma_f32 v75, v82, v82, v75
	v_add_f32_dpp v89, v57, v57 wave_shr:1 row_mask:0xf bank_mask:0xf bound_ctrl:1
	v_add_f32_e64 v88, v88, v86
	v_pk_fma_f32 v[66:67], v[84:85], v[84:85], v[66:67] op_sel_hi:[0,1,1]
	v_pk_fma_f32 v[70:71], v[84:85], v[86:87], v[70:71] op_sel_hi:[1,0,1]
	v_fma_f32 v74, v85, v85, v74
	v_fma_f32 v75, v86, v86, v75
	v_add_f32_dpp v89, v57, v89 wave_shl:1 row_mask:0xf bank_mask:0xf bound_ctrl:1
	v_mov_b32_dpp v92, v6 wave_shr:1 row_mask:0xf bank_mask:0xf bound_ctrl:1
	v_mov_b32_dpp v93, v7 wave_shr:1 row_mask:0xf bank_mask:0xf bound_ctrl:1
	v_mov_b32_dpp v96, v6 wave_shl:1 row_mask:0xf bank_mask:0xf bound_ctrl:1
	v_mov_b32_dpp v97, v7 wave_shl:1 row_mask:0xf bank_mask:0xf bound_ctrl:1
	v_pk_mul_f32 v[90:91], v[6:7], v[12:13] op_sel_hi:[1,0]
	v_pk_mul_f32 v[94:95], v[6:7], v[12:13] op_sel:[0,1]
	v_pk_mul_f32 v[98:99], v[6:7], v[14:15] op_sel_hi:[1,0]
	v_pk_add_f32 v[102:103], v[6:7], v[92:93]
	v_pk_fma_f32 v[90:91], v[92:93], v[80:81], v[90:91] op_sel_hi:[1,0,1]
	v_pk_fma_f32 v[94:95], v[92:93], v[80:81], v[94:95] op_sel:[0,1,0]
	v_pk_fma_f32 v[98:99], v[92:93], v[82:83], v[98:99] op_sel_hi:[1,0,1]
	v_pk_add_f32 v[102:103], v[102:103], v[96:97]
	v_pk_fma_f32 v[90:91], v[96:97], v[84:85], v[90:91] op_sel_hi:[1,0,1]
	v_pk_fma_f32 v[94:95], v[96:97], v[84:85], v[94:95] op_sel:[0,1,0]
	v_pk_fma_f32 v[98:99], v[96:97], v[86:87], v[98:99] op_sel_hi:[1,0,1]
	s_barrier
	s_add_i32 s5, s34, 2
	s_min_i32 s5, s5, 0x200
	s_mul_i32 s6, s5, 0x804
	s_add_i32 s6, s6, s35
	s_add_i32 s7, s6, 0x505014
	s_add_i32 s8, s6, 0x606018
	s_mul_i32 s9, s5, 0x180c
	s_add_i32 s9, s9, s33
	s_add_i32 s4, s34, 3
	s_min_i32 s4, s4, 0x200
	s_mul_i32 s4, s4, 0x804
	s_add_i32 s4, s4, s38
	buffer_load_dword v24, v28, s[20:23], s4 offen nt
	buffer_load_dwordx3 v[104:106], v27, s[24:27], s9 offen nt
	buffer_load_dword v92, v28, s[16:19], s7 offen nt
	buffer_load_dword v93, v28, s[16:19], s8 offen nt
	s_waitcnt vmcnt(8)
	s_add_i32 s4, s34, 1
	s_cmpk_lt_u32 s4, 0x201
	s_cselect_b64 s[12:13], s[40:41], 0
	v_cmp_eq_u32_e64 s[14:15], s37, v17
	s_and_b64 s[14:15], s[14:15], s[12:13]
	v_cndmask_b32_e64 v29, 0, 1, s[14:15]
	v_mov_b32_dpp v108, v32 wave_shr:1 row_mask:0xf bank_mask:0xf bound_ctrl:1
	v_mov_b32_dpp v109, v33 wave_shr:1 row_mask:0xf bank_mask:0xf bound_ctrl:1
	v_or_b32_dpp v57, v29, v29 wave_shr:1 row_mask:0xf bank_mask:0xf bound_ctrl:1
	v_mov_b32_dpp v110, v34 wave_shr:1 row_mask:0xf bank_mask:0xf bound_ctrl:1
	v_or_b32_dpp v57, v29, v57 wave_shl:1 row_mask:0xf bank_mask:0xf bound_ctrl:1
	v_mov_b32_dpp v112, v32 wave_shl:1 row_mask:0xf bank_mask:0xf bound_ctrl:1
	v_mov_b32_dpp v113, v33 wave_shl:1 row_mask:0xf bank_mask:0xf bound_ctrl:1
	v_or_b32_dpp v58, v57, v57 wave_shr:1 row_mask:0xf bank_mask:0xf bound_ctrl:1
	v_mov_b32_dpp v114, v34 wave_shl:1 row_mask:0xf bank_mask:0xf bound_ctrl:1
	v_or_b32_dpp v58, v57, v58 wave_shl:1 row_mask:0xf bank_mask:0xf bound_ctrl:1
	s_waitcnt vmcnt(8)
	v_pk_add_f32 v[96:97], v[32:33], v[108:109]
	v_pk_mul_f32 v[100:101], v[32:33], v[32:33] op_sel_hi:[0,1]
	v_pk_mul_f32 v[116:117], v[32:33], v[34:35] op_sel_hi:[1,0]
	v_mul_f32_e64 v118, v33, v33
	v_mul_f32_e64 v119, v34, v34
	v_add_f32_e64 v120, v34, v110
	v_pk_add_f32 v[96:97], v[96:97], v[112:113]
	v_or3_b32 v29, v58, v59, v56
	v_or3_b32 v29, v29, v37, v36
	s_add_i32 s4, s34, -2
	s_cmpk_lt_u32 s4, 0x1ff
	s_cselect_b64 s[12:13], s[42:43], 0
	v_cmp_ne_u32_e64 s[30:31], 0, v29
	s_and_b64 s[30:31], s[30:31], s[12:13]
	v_cndmask_b32_e64 v29, 0, 1.0, s[30:31]
	v_pk_fma_f32 v[100:101], v[108:109], v[108:109], v[100:101] op_sel_hi:[0,1,1]
	v_pk_fma_f32 v[116:117], v[108:109], v[110:111], v[116:117] op_sel_hi:[1,0,1]
	v_fma_f32 v118, v109, v109, v118
	v_fma_f32 v119, v110, v110, v119
	v_add_f32_dpp v121, v29, v29 wave_shr:1 row_mask:0xf bank_mask:0xf bound_ctrl:1
	v_add_f32_e64 v120, v120, v114
	v_pk_fma_f32 v[100:101], v[112:113], v[112:113], v[100:101] op_sel_hi:[0,1,1]
	v_pk_fma_f32 v[116:117], v[112:113], v[114:115], v[116:117] op_sel_hi:[1,0,1]
	v_fma_f32 v118, v113, v113, v118
	v_fma_f32 v119, v114, v114, v119
	v_add_f32_dpp v121, v29, v121 wave_shl:1 row_mask:0xf bank_mask:0xf bound_ctrl:1
	v_pk_add_f32 v[124:125], v[62:63], v[96:97]
	v_pk_add_f32 v[122:123], v[38:39], v[124:125]
	v_pk_add_f32 v[38:39], v[66:67], v[100:101]
	v_pk_add_f32 v[62:63], v[48:49], v[38:39]
	v_pk_add_f32 v[48:49], v[70:71], v[116:117]
	v_pk_add_f32 v[66:67], v[50:51], v[48:49]
	v_pk_add_f32 v[50:51], v[74:75], v[118:119]
	v_pk_add_f32 v[70:71], v[52:53], v[50:51]
	v_pk_add_f32 v[52:53], v[88:89], v[120:121]
	v_pk_add_f32 v[74:75], v[54:55], v[52:53]
	v_mul_f32_e64 v128, v122, v22
	v_mul_f32_e64 v129, v123, v22
	v_mul_f32_e64 v130, v74, v22
	v_fma_f32 v29, v62, v22, v26
	v_mul_f32_e64 v57, v63, v22
	v_mul_f32_e64 v54, v66, v22
	v_fma_f32 v55, v70, v22, v26
	v_mul_f32_e64 v88, v67, v22
	v_fma_f32 v89, v71, v22, v26
	v_fma_f32 v29, -v128, v128, v29
	v_fma_f32 v57, -v128, v129, v57
	v_fma_f32 v54, -v128, v130, v54
	v_fma_f32 v55, -v129, v129, v55
	v_fma_f32 v88, -v129, v130, v88
	v_fma_f32 v89, -v130, v130, v89
	v_mul_f32_e64 v126, v88, v88
	v_mul_f32_e64 v127, v57, v89
	v_mul_f32_e64 v140, v54, v55
	v_mul_f32_e64 v141, v54, v54
	v_mul_f32_e64 v142, v29, v88
	v_mul_f32_e64 v143, v57, v57
	v_fma_f32 v126, v55, v89, -v126
	v_fma_f32 v127, v54, v88, -v127
	v_fma_f32 v140, v57, v88, -v140
	v_fma_f32 v141, v29, v89, -v141
	v_fma_f32 v142, v57, v54, -v142
	v_fma_f32 v143, v29, v55, -v143
	v_mul_f32_e64 v144, v29, v126
	v_fma_f32 v144, v57, v127, v144
	v_fma_f32 v144, v54, v140, v144
	v_rcp_f32_e32 v144, v144
	v_cmp_ne_u32_e64 vcc, s37, v2
	v_mul_f32_e64 v144, v144, v22
	v_cndmask_b32_e64 v144, 0, v144, s[30:31]
	v_cndmask_b32_e64 v29, 0, v18, vcc
	v_cndmask_b32_e64 v137, 0, v22, s[30:31]
	v_mul_f32_e64 v131, v126, v144
	v_mul_f32_e64 v132, v127, v144
	v_mul_f32_e64 v133, v140, v144
	v_mul_f32_e64 v134, v141, v144
	v_mul_f32_e64 v135, v142, v144
	v_mul_f32_e64 v136, v143, v144
	v_add_f32_e64 v138, v75, v29
	v_mov_b32_e32 v139, v2
	ds_write_b128 v23, v[128:131]
	ds_write_b128 v23, v[132:135] offset:1024
	ds_write_b128 v23, v[136:139] offset:2048
	v_mov_b32_dpp v54, v20 wave_shr:1 row_mask:0xf bank_mask:0xf bound_ctrl:1
	v_mov_b32_dpp v55, v21 wave_shr:1 row_mask:0xf bank_mask:0xf bound_ctrl:1
	v_mov_b32_dpp v62, v20 wave_shl:1 row_mask:0xf bank_mask:0xf bound_ctrl:1
	v_mov_b32_dpp v63, v21 wave_shl:1 row_mask:0xf bank_mask:0xf bound_ctrl:1
	v_pk_mul_f32 v[88:89], v[20:21], v[32:33] op_sel_hi:[1,0]
	v_pk_mul_f32 v[140:141], v[20:21], v[32:33] op_sel:[0,1]
	v_pk_mul_f32 v[144:145], v[20:21], v[34:35] op_sel_hi:[1,0]
	v_pk_add_f32 v[148:149], v[20:21], v[54:55]
	v_pk_fma_f32 v[88:89], v[54:55], v[108:109], v[88:89] op_sel_hi:[1,0,1]
	v_pk_fma_f32 v[140:141], v[54:55], v[108:109], v[140:141] op_sel:[0,1,0]
	v_pk_fma_f32 v[144:145], v[54:55], v[110:111], v[144:145] op_sel_hi:[1,0,1]
	v_pk_add_f32 v[148:149], v[148:149], v[62:63]
	v_pk_fma_f32 v[88:89], v[62:63], v[112:113], v[88:89] op_sel_hi:[1,0,1]
	v_pk_fma_f32 v[140:141], v[62:63], v[112:113], v[140:141] op_sel:[0,1,0]
	v_pk_fma_f32 v[144:145], v[62:63], v[114:115], v[144:145] op_sel_hi:[1,0,1]
	s_waitcnt lgkmcnt(0)
	s_barrier
	s_add_i32 s5, s34, 3
	s_min_i32 s5, s5, 0x200
	s_mul_i32 s6, s5, 0x804
	s_add_i32 s6, s6, s35
	s_add_i32 s7, s6, 0x505014
	s_add_i32 s8, s6, 0x606018
	s_mul_i32 s9, s5, 0x180c
	s_add_i32 s9, s9, s33
	s_add_i32 s4, s34, 4
	s_min_i32 s4, s4, 0x200
	s_mul_i32 s4, s4, 0x804
	s_add_i32 s4, s4, s38
	buffer_load_dword v2, v28, s[20:23], s4 offen nt
	buffer_load_dwordx3 v[152:154], v27, s[24:27], s9 offen nt
	buffer_load_dword v54, v28, s[16:19], s7 offen nt
	buffer_load_dword v55, v28, s[16:19], s8 offen nt
	s_waitcnt vmcnt(8)
	s_add_i32 s4, s34, 2
	s_cmpk_lt_u32 s4, 0x201
	s_cselect_b64 s[12:13], s[40:41], 0
	v_cmp_eq_u32_e64 s[14:15], s37, v25
	s_and_b64 s[14:15], s[14:15], s[12:13]
	v_cndmask_b32_e64 v29, 0, 1, s[14:15]
	v_mov_b32_dpp v156, v76 wave_shr:1 row_mask:0xf bank_mask:0xf bound_ctrl:1
	v_mov_b32_dpp v157, v77 wave_shr:1 row_mask:0xf bank_mask:0xf bound_ctrl:1
	v_or_b32_dpp v36, v29, v29 wave_shr:1 row_mask:0xf bank_mask:0xf bound_ctrl:1
	v_mov_b32_dpp v158, v78 wave_shr:1 row_mask:0xf bank_mask:0xf bound_ctrl:1
	v_or_b32_dpp v36, v29, v36 wave_shl:1 row_mask:0xf bank_mask:0xf bound_ctrl:1
	v_mov_b32_dpp v160, v76 wave_shl:1 row_mask:0xf bank_mask:0xf bound_ctrl:1
	v_mov_b32_dpp v161, v77 wave_shl:1 row_mask:0xf bank_mask:0xf bound_ctrl:1
	v_or_b32_dpp v57, v36, v36 wave_shr:1 row_mask:0xf bank_mask:0xf bound_ctrl:1
	v_mov_b32_dpp v162, v78 wave_shl:1 row_mask:0xf bank_mask:0xf bound_ctrl:1
	v_or_b32_dpp v57, v36, v57 wave_shl:1 row_mask:0xf bank_mask:0xf bound_ctrl:1
	v_pk_add_f32 v[62:63], v[102:103], v[148:149]
	v_pk_add_f32 v[66:67], v[72:73], v[62:63]
	v_pk_add_f32 v[70:71], v[90:91], v[88:89]
	v_pk_add_f32 v[72:73], v[60:61], v[70:71]
	v_pk_add_f32 v[74:75], v[94:95], v[140:141]
	v_pk_add_f32 v[60:61], v[64:65], v[74:75]
	v_pk_add_f32 v[90:91], v[98:99], v[144:145]
	v_pk_add_f32 v[64:65], v[68:69], v[90:91]
	v_pk_fma_f32 v[72:73], v[128:129], v[66:67], v[72:73] op_sel_hi:[0,1,1] neg_lo:[1,0,0] neg_hi:[1,0,0]
	v_pk_fma_f32 v[60:61], v[128:129], v[66:67], v[60:61] op_sel:[1,0,0] neg_lo:[1,0,0] neg_hi:[1,0,0]
	v_pk_fma_f32 v[64:65], v[130:131], v[66:67], v[64:65] op_sel_hi:[0,1,1] neg_lo:[1,0,0] neg_hi:[1,0,0]
	v_pk_mul_f32 v[94:95], v[130:131], v[72:73] op_sel:[1,0]
	v_pk_mul_f32 v[98:99], v[132:133], v[72:73] op_sel_hi:[0,1]
	v_pk_mul_f32 v[102:103], v[132:133], v[72:73] op_sel:[1,0]
	v_pk_fma_f32 v[94:95], v[132:133], v[60:61], v[94:95] op_sel_hi:[0,1,1]
	v_pk_fma_f32 v[98:99], v[134:135], v[60:61], v[98:99] op_sel_hi:[0,1,1]
	v_pk_fma_f32 v[102:103], v[134:135], v[60:61], v[102:103] op_sel:[1,0,0]
	v_pk_fma_f32 v[94:95], v[132:133], v[64:65], v[94:95] op_sel:[1,0,0]
	v_pk_fma_f32 v[98:99], v[134:135], v[64:65], v[98:99] op_sel:[1,0,0]
	v_pk_fma_f32 v[102:103], v[136:137], v[64:65], v[102:103] op_sel_hi:[0,1,1]
	v_pk_mul_f32 v[68:69], v[128:129], v[94:95] op_sel_hi:[0,1]
	v_pk_fma_f32 v[68:69], v[128:129], v[98:99], v[68:69] op_sel:[1,0,0]
	v_pk_fma_f32 v[68:69], v[130:131], v[102:103], v[68:69] op_sel_hi:[0,1,1]
	v_pk_fma_f32 v[68:69], v[136:137], v[66:67], v[68:69] op_sel:[1,0,0] neg_lo:[0,0,1] neg_hi:[0,0,1]
	s_waitcnt vmcnt(8)
	v_pk_add_f32 v[4:5], v[76:77], v[156:157]
	v_pk_mul_f32 v[8:9], v[76:77], v[76:77] op_sel_hi:[0,1]
	v_pk_mul_f32 v[10:11], v[76:77], v[78:79] op_sel_hi:[1,0]
	v_mul_f32_e64 v40, v77, v77
	v_mul_f32_e64 v41, v78, v78
	v_add_f32_e64 v42, v78, v158
	v_pk_add_f32 v[4:5], v[4:5], v[160:161]
	v_or3_b32 v29, v57, v58, v59
	v_or3_b32 v29, v29, v56, v37
	s_add_i32 s4, s34, -1
	s_cmpk_lt_u32 s4, 0x1ff
	s_cselect_b64 s[12:13], s[42:43], 0
	v_cmp_ne_u32_e64 s[30:31], 0, v29
	s_and_b64 s[30:31], s[30:31], s[12:13]
	v_cndmask_b32_e64 v29, 0, 1.0, s[30:31]
	v_pk_fma_f32 v[8:9], v[156:157], v[156:157], v[8:9] op_sel_hi:[0,1,1]
	v_pk_fma_f32 v[10:11], v[156:157], v[158:159], v[10:11] op_sel_hi:[1,0,1]
	v_fma_f32 v40, v157, v157, v40
	v_fma_f32 v41, v158, v158, v41
	v_add_f32_dpp v43, v29, v29 wave_shr:1 row_mask:0xf bank_mask:0xf bound_ctrl:1
	v_add_f32_e64 v42, v42, v162
	v_pk_fma_f32 v[8:9], v[160:161], v[160:161], v[8:9] op_sel_hi:[0,1,1]
	v_pk_fma_f32 v[10:11], v[160:161], v[162:163], v[10:11] op_sel_hi:[1,0,1]
	v_fma_f32 v40, v161, v161, v40
	v_fma_f32 v41, v162, v162, v41
	v_add_f32_dpp v43, v29, v43 wave_shl:1 row_mask:0xf bank_mask:0xf bound_ctrl:1
	v_pk_add_f32 v[44:45], v[124:125], v[4:5]
	v_pk_add_f32 v[46:47], v[38:39], v[8:9]
	v_pk_add_f32 v[38:39], v[48:49], v[10:11]
	v_pk_add_f32 v[48:49], v[50:51], v[40:41]
	v_pk_add_f32 v[50:51], v[52:53], v[42:43]
	v_mul_f32_e64 v64, v44, v22
	v_mul_f32_e64 v65, v45, v22
	v_mul_f32_e64 v66, v50, v22
	v_fma_f32 v29, v46, v22, v26
	v_mul_f32_e64 v36, v47, v22
	v_mul_f32_e64 v52, v38, v22
	v_fma_f32 v53, v48, v22, v26
	v_mul_f32_e64 v60, v39, v22
	v_fma_f32 v61, v49, v22, v26
	v_fma_f32 v29, -v64, v64, v29
	v_fma_f32 v36, -v64, v65, v36
	v_fma_f32 v52, -v64, v66, v52
	v_fma_f32 v53, -v65, v65, v53
	v_fma_f32 v60, -v65, v66, v60
	v_fma_f32 v61, -v66, v66, v61
	v_mul_f32_e64 v72, v60, v60
	v_mul_f32_e64 v73, v36, v61
	v_mul_f32_e64 v122, v52, v53
	v_mul_f32_e64 v123, v52, v52
	v_mul_f32_e64 v132, v29, v60
	v_mul_f32_e64 v133, v36, v36
	v_fma_f32 v72, v53, v61, -v72
	v_fma_f32 v73, v52, v60, -v73
	v_fma_f32 v122, v36, v60, -v122
	v_fma_f32 v123, v29, v61, -v123
	v_fma_f32 v132, v36, v52, -v132
	v_fma_f32 v133, v29, v53, -v133
	v_mul_f32_e64 v134, v29, v72
	v_fma_f32 v134, v36, v73, v134
	v_fma_f32 v134, v52, v122, v134
	v_rcp_f32_e32 v134, v134
	v_cmp_ne_u32_e64 vcc, s37, v3
	v_mul_f32_e64 v134, v134, v22
	v_cndmask_b32_e64 v134, 0, v134, s[30:31]
	v_cndmask_b32_e64 v29, 0, v18, vcc
	v_cndmask_b32_e64 v129, 0, v22, s[30:31]
	v_mul_f32_e64 v67, v72, v134
	v_mul_f32_e64 v124, v73, v134
	v_mul_f32_e64 v125, v122, v134
	v_mul_f32_e64 v126, v123, v134
	v_mul_f32_e64 v127, v132, v134
	v_mul_f32_e64 v128, v133, v134
	v_add_f32_e64 v130, v51, v29
	v_mov_b32_e32 v131, v3
	ds_write_b128 v23, v[64:67] offset:3072
	ds_write_b128 v23, v[124:127] offset:4096
	ds_write_b128 v23, v[128:131] offset:5120
	v_mov_b32_dpp v36, v30 wave_shr:1 row_mask:0xf bank_mask:0xf bound_ctrl:1
	v_mov_b32_dpp v37, v31 wave_shr:1 row_mask:0xf bank_mask:0xf bound_ctrl:1
	v_mov_b32_dpp v44, v30 wave_shl:1 row_mask:0xf bank_mask:0xf bound_ctrl:1
	v_mov_b32_dpp v45, v31 wave_shl:1 row_mask:0xf bank_mask:0xf bound_ctrl:1
	v_pk_mul_f32 v[38:39], v[30:31], v[76:77] op_sel_hi:[1,0]
	v_pk_mul_f32 v[46:47], v[30:31], v[76:77] op_sel:[0,1]
	v_pk_mul_f32 v[50:51], v[30:31], v[78:79] op_sel_hi:[1,0]
	v_pk_add_f32 v[122:123], v[30:31], v[36:37]
	v_pk_fma_f32 v[38:39], v[36:37], v[156:157], v[38:39] op_sel_hi:[1,0,1]
	v_pk_fma_f32 v[46:47], v[36:37], v[156:157], v[46:47] op_sel:[0,1,0]
	v_pk_fma_f32 v[50:51], v[36:37], v[158:159], v[50:51] op_sel_hi:[1,0,1]
	v_pk_add_f32 v[122:123], v[122:123], v[44:45]
	v_pk_fma_f32 v[38:39], v[44:45], v[160:161], v[38:39] op_sel_hi:[1,0,1]
	v_pk_fma_f32 v[46:47], v[44:45], v[160:161], v[46:47] op_sel:[0,1,0]
	v_pk_fma_f32 v[50:51], v[44:45], v[162:163], v[50:51] op_sel_hi:[1,0,1]
	s_waitcnt lgkmcnt(0)
	s_barrier
	s_add_i32 s5, s34, 4
	s_min_i32 s5, s5, 0x200
	s_mul_i32 s6, s5, 0x804
	s_add_i32 s6, s6, s35
	s_add_i32 s7, s6, 0x505014
	s_add_i32 s8, s6, 0x606018
	s_mul_i32 s9, s5, 0x180c
	s_add_i32 s9, s9, s33
	s_add_i32 s4, s34, 5
	s_min_i32 s4, s4, 0x200
	s_mul_i32 s4, s4, 0x804
	s_add_i32 s4, s4, s38
	buffer_load_dword v3, v28, s[20:23], s4 offen nt
	buffer_load_dwordx3 v[132:134], v27, s[24:27], s9 offen nt
	buffer_load_dword v36, v28, s[16:19], s7 offen nt
	buffer_load_dword v37, v28, s[16:19], s8 offen nt
	s_waitcnt vmcnt(8)
	s_add_i32 s4, s34, 3
	s_cmpk_lt_u32 s4, 0x201
	s_cselect_b64 s[12:13], s[40:41], 0
	v_cmp_eq_u32_e64 s[14:15], s37, v24
	s_and_b64 s[14:15], s[14:15], s[12:13]
	v_cndmask_b32_e64 v29, 0, 1, s[14:15]
	v_mov_b32_dpp v136, v104 wave_shr:1 row_mask:0xf bank_mask:0xf bound_ctrl:1
	v_mov_b32_dpp v137, v105 wave_shr:1 row_mask:0xf bank_mask:0xf bound_ctrl:1
	v_or_b32_dpp v44, v29, v29 wave_shr:1 row_mask:0xf bank_mask:0xf bound_ctrl:1
	v_mov_b32_dpp v138, v106 wave_shr:1 row_mask:0xf bank_mask:0xf bound_ctrl:1
	v_or_b32_dpp v44, v29, v44 wave_shl:1 row_mask:0xf bank_mask:0xf bound_ctrl:1
	v_mov_b32_dpp v164, v104 wave_shl:1 row_mask:0xf bank_mask:0xf bound_ctrl:1
	v_mov_b32_dpp v165, v105 wave_shl:1 row_mask:0xf bank_mask:0xf bound_ctrl:1
	v_or_b32_dpp v45, v44, v44 wave_shr:1 row_mask:0xf bank_mask:0xf bound_ctrl:1
	v_mov_b32_dpp v166, v106 wave_shl:1 row_mask:0xf bank_mask:0xf bound_ctrl:1
	v_or_b32_dpp v45, v44, v45 wave_shl:1 row_mask:0xf bank_mask:0xf bound_ctrl:1
	v_pk_add_f32 v[48:49], v[62:63], v[122:123]
	v_pk_add_f32 v[62:63], v[70:71], v[38:39]
	v_pk_add_f32 v[70:71], v[74:75], v[46:47]
	v_pk_add_f32 v[74:75], v[90:91], v[50:51]
	v_pk_fma_f32 v[62:63], v[64:65], v[48:49], v[62:63] op_sel_hi:[0,1,1] neg_lo:[1,0,0] neg_hi:[1,0,0]
	v_pk_fma_f32 v[70:71], v[64:65], v[48:49], v[70:71] op_sel:[1,0,0] neg_lo:[1,0,0] neg_hi:[1,0,0]
	v_pk_fma_f32 v[74:75], v[66:67], v[48:49], v[74:75] op_sel_hi:[0,1,1] neg_lo:[1,0,0] neg_hi:[1,0,0]
	v_pk_mul_f32 v[52:53], v[66:67], v[62:63] op_sel:[1,0]
	v_pk_mul_f32 v[60:61], v[124:125], v[62:63] op_sel_hi:[0,1]
	v_pk_mul_f32 v[72:73], v[124:125], v[62:63] op_sel:[1,0]
	v_pk_fma_f32 v[52:53], v[124:125], v[70:71], v[52:53] op_sel_hi:[0,1,1]
	v_pk_fma_f32 v[60:61], v[126:127], v[70:71], v[60:61] op_sel_hi:[0,1,1]
	v_pk_fma_f32 v[72:73], v[126:127], v[70:71], v[72:73] op_sel:[1,0,0]
	v_pk_fma_f32 v[52:53], v[124:125], v[74:75], v[52:53] op_sel:[1,0,0]
	v_pk_fma_f32 v[60:61], v[126:127], v[74:75], v[60:61] op_sel:[1,0,0]
	v_pk_fma_f32 v[72:73], v[128:129], v[74:75], v[72:73] op_sel_hi:[0,1,1]
	v_pk_mul_f32 v[90:91], v[64:65], v[52:53] op_sel_hi:[0,1]
	v_pk_fma_f32 v[90:91], v[64:65], v[60:61], v[90:91] op_sel:[1,0,0]
	v_pk_fma_f32 v[90:91], v[66:67], v[72:73], v[90:91] op_sel_hi:[0,1,1]
	v_pk_fma_f32 v[90:91], v[128:129], v[48:49], v[90:91] op_sel:[1,0,0] neg_lo:[0,0,1] neg_hi:[0,0,1]
	s_waitcnt vmcnt(8)
	v_pk_add_f32 v[6:7], v[104:105], v[136:137]
	v_pk_mul_f32 v[12:13], v[104:105], v[104:105] op_sel_hi:[0,1]
	v_pk_mul_f32 v[14:15], v[104:105], v[106:107] op_sel_hi:[1,0]
	v_mul_f32_e64 v48, v105, v105
	v_mul_f32_e64 v49, v106, v106
	v_add_f32_e64 v62, v106, v138
	v_pk_add_f32 v[6:7], v[6:7], v[164:165]
	v_or3_b32 v29, v45, v57, v58
	v_or3_b32 v29, v29, v59, v56
	s_add_i32 s4, s34, 0
	s_cmpk_lt_u32 s4, 0x1ff
	s_cselect_b64 s[12:13], s[42:43], 0
	v_cmp_ne_u32_e64 s[30:31], 0, v29
	s_and_b64 s[30:31], s[30:31], s[12:13]
	v_cndmask_b32_e64 v29, 0, 1.0, s[30:31]
	v_pk_fma_f32 v[12:13], v[136:137], v[136:137], v[12:13] op_sel_hi:[0,1,1]
	v_pk_fma_f32 v[14:15], v[136:137], v[138:139], v[14:15] op_sel_hi:[1,0,1]
	v_fma_f32 v48, v137, v137, v48
	v_fma_f32 v49, v138, v138, v49
	v_add_f32_dpp v63, v29, v29 wave_shr:1 row_mask:0xf bank_mask:0xf bound_ctrl:1
	v_add_f32_e64 v62, v62, v166
	v_pk_fma_f32 v[12:13], v[164:165], v[164:165], v[12:13] op_sel_hi:[0,1,1]
	v_pk_fma_f32 v[14:15], v[164:165], v[166:167], v[14:15] op_sel_hi:[1,0,1]
	v_fma_f32 v48, v165, v165, v48
	v_fma_f32 v49, v166, v166, v49
	v_add_f32_dpp v63, v29, v63 wave_shl:1 row_mask:0xf bank_mask:0xf bound_ctrl:1
	v_pk_add_f32 v[66:67], v[4:5], v[6:7]
	v_pk_add_f32 v[64:65], v[96:97], v[66:67]
	v_pk_add_f32 v[70:71], v[8:9], v[12:13]
	v_pk_add_f32 v[4:5], v[100:101], v[70:71]
	v_pk_add_f32 v[74:75], v[10:11], v[14:15]
	v_pk_add_f32 v[8:9], v[116:117], v[74:75]
	v_pk_add_f32 v[80:81], v[40:41], v[48:49]
	v_pk_add_f32 v[10:11], v[118:119], v[80:81]
	v_pk_add_f32 v[82:83], v[42:43], v[62:63]
	v_pk_add_f32 v[40:41], v[120:121], v[82:83]
	v_mul_f32_e64 v84, v64, v22
	v_mul_f32_e64 v85, v65, v22
	v_mul_f32_e64 v86, v40, v22
	v_fma_f32 v29, v4, v22, v26
	v_mul_f32_e64 v44, v5, v22
	v_mul_f32_e64 v42, v8, v22
	v_fma_f32 v43, v10, v22, v26
	v_mul_f32_e64 v96, v9, v22
	v_fma_f32 v97, v11, v22, v26
	v_fma_f32 v29, -v84, v84, v29
	v_fma_f32 v44, -v84, v85, v44
	v_fma_f32 v42, -v84, v86, v42
	v_fma_f32 v43, -v85, v85, v43
	v_fma_f32 v96, -v85, v86, v96
	v_fma_f32 v97, -v86, v86, v97
	v_mul_f32_e64 v100, v96, v96
	v_mul_f32_e64 v101, v44, v97
	v_mul_f32_e64 v120, v42, v43
	v_mul_f32_e64 v121, v42, v42
	v_mul_f32_e64 v128, v29, v96
	v_mul_f32_e64 v129, v44, v44
	v_fma_f32 v100, v43, v97, -v100
	v_fma_f32 v101, v42, v96, -v101
	v_fma_f32 v120, v44, v96, -v120
	v_fma_f32 v121, v29, v97, -v121
	v_fma_f32 v128, v44, v42, -v128
	v_fma_f32 v129, v29, v43, -v129
	v_mul_f32_e64 v130, v29, v100
	v_fma_f32 v130, v44, v101, v130
	v_fma_f32 v130, v42, v120, v130
	v_rcp_f32_e32 v130, v130
	v_cmp_ne_u32_e64 vcc, s37, v16
	v_mul_f32_e64 v130, v130, v22
	v_cndmask_b32_e64 v130, 0, v130, s[30:31]
	v_cndmask_b32_e64 v29, 0, v18, vcc
	v_cndmask_b32_e64 v125, 0, v22, s[30:31]
	v_mul_f32_e64 v87, v100, v130
	v_mul_f32_e64 v116, v101, v130
	v_mul_f32_e64 v117, v120, v130
	v_mul_f32_e64 v118, v121, v130
	v_mul_f32_e64 v119, v128, v130
	v_mul_f32_e64 v124, v129, v130
	v_add_f32_e64 v126, v41, v29
	v_mov_b32_e32 v127, v16
	ds_write_b128 v23, v[84:87]
	ds_write_b128 v23, v[116:119] offset:1024
	ds_write_b128 v23, v[124:127] offset:2048
	v_mov_b32_dpp v10, v92 wave_shr:1 row_mask:0xf bank_mask:0xf bound_ctrl:1
	v_mov_b32_dpp v11, v93 wave_shr:1 row_mask:0xf bank_mask:0xf bound_ctrl:1
	v_mov_b32_dpp v42, v92 wave_shl:1 row_mask:0xf bank_mask:0xf bound_ctrl:1
	v_mov_b32_dpp v43, v93 wave_shl:1 row_mask:0xf bank_mask:0xf bound_ctrl:1
	v_pk_mul_f32 v[4:5], v[92:93], v[104:105] op_sel_hi:[1,0]
	v_pk_mul_f32 v[8:9], v[92:93], v[104:105] op_sel:[0,1]
	v_pk_mul_f32 v[40:41], v[92:93], v[106:107] op_sel_hi:[1,0]
	v_pk_add_f32 v[64:65], v[92:93], v[10:11]
	v_pk_fma_f32 v[4:5], v[10:11], v[136:137], v[4:5] op_sel_hi:[1,0,1]
	v_pk_fma_f32 v[8:9], v[10:11], v[136:137], v[8:9] op_sel:[0,1,0]
	v_pk_fma_f32 v[40:41], v[10:11], v[138:139], v[40:41] op_sel_hi:[1,0,1]
	v_pk_add_f32 v[64:65], v[64:65], v[42:43]
	v_pk_fma_f32 v[4:5], v[42:43], v[164:165], v[4:5] op_sel_hi:[1,0,1]
	v_pk_fma_f32 v[8:9], v[42:43], v[164:165], v[8:9] op_sel:[0,1,0]
	v_pk_fma_f32 v[40:41], v[42:43], v[166:167], v[40:41] op_sel_hi:[1,0,1]
	s_waitcnt lgkmcnt(0)
	s_barrier
	s_add_i32 s5, s34, 5
	s_min_i32 s5, s5, 0x200
	s_mul_i32 s6, s5, 0x804
	s_add_i32 s6, s6, s35
	s_add_i32 s7, s6, 0x505014
	s_add_i32 s8, s6, 0x606018
	s_mul_i32 s9, s5, 0x180c
	s_add_i32 s9, s9, s33
	s_add_i32 s4, s34, 6
	s_min_i32 s4, s4, 0x200
	s_mul_i32 s4, s4, 0x804
	s_add_i32 s4, s4, s38
	buffer_load_dword v16, v28, s[20:23], s4 offen nt
	buffer_load_dwordx3 v[128:130], v27, s[24:27], s9 offen nt
	buffer_load_dword v10, v28, s[16:19], s7 offen nt
	buffer_load_dword v11, v28, s[16:19], s8 offen nt
	s_waitcnt vmcnt(8)
	s_add_i32 s4, s34, 4
	s_cmpk_lt_u32 s4, 0x201
	s_cselect_b64 s[12:13], s[40:41], 0
	v_cmp_eq_u32_e64 s[14:15], s37, v2
	s_and_b64 s[14:15], s[14:15], s[12:13]
	v_cndmask_b32_e64 v29, 0, 1, s[14:15]
	v_mov_b32_dpp v168, v152 wave_shr:1 row_mask:0xf bank_mask:0xf bound_ctrl:1
	v_mov_b32_dpp v169, v153 wave_shr:1 row_mask:0xf bank_mask:0xf bound_ctrl:1
	v_or_b32_dpp v44, v29, v29 wave_shr:1 row_mask:0xf bank_mask:0xf bound_ctrl:1
	v_mov_b32_dpp v170, v154 wave_shr:1 row_mask:0xf bank_mask:0xf bound_ctrl:1
	v_or_b32_dpp v44, v29, v44 wave_shl:1 row_mask:0xf bank_mask:0xf bound_ctrl:1
	v_mov_b32_dpp v172, v152 wave_shl:1 row_mask:0xf bank_mask:0xf bound_ctrl:1
	v_mov_b32_dpp v173, v153 wave_shl:1 row_mask:0xf bank_mask:0xf bound_ctrl:1
	v_or_b32_dpp v56, v44, v44 wave_shr:1 row_mask:0xf bank_mask:0xf bound_ctrl:1
	v_mov_b32_dpp v174, v154 wave_shl:1 row_mask:0xf bank_mask:0xf bound_ctrl:1
	v_or_b32_dpp v56, v44, v56 wave_shl:1 row_mask:0xf bank_mask:0xf bound_ctrl:1
	v_pk_add_f32 v[42:43], v[122:123], v[64:65]
	v_pk_add_f32 v[96:97], v[148:149], v[42:43]
	v_pk_add_f32 v[122:123], v[38:39], v[4:5]
	v_pk_add_f32 v[142:143], v[88:89], v[122:123]
	v_pk_add_f32 v[38:39], v[46:47], v[8:9]
	v_pk_add_f32 v[146:147], v[140:141], v[38:39]
	v_pk_add_f32 v[46:47], v[50:51], v[40:41]
	v_pk_add_f32 v[150:151], v[144:145], v[46:47]
	v_pk_fma_f32 v[142:143], v[84:85], v[96:97], v[142:143] op_sel_hi:[0,1,1] neg_lo:[1,0,0] neg_hi:[1,0,0]
	v_pk_fma_f32 v[146:147], v[84:85], v[96:97], v[146:147] op_sel:[1,0,0] neg_lo:[1,0,0] neg_hi:[1,0,0]
	v_pk_fma_f32 v[150:151], v[86:87], v[96:97], v[150:151] op_sel_hi:[0,1,1] neg_lo:[1,0,0] neg_hi:[1,0,0]
	v_pk_mul_f32 v[88:89], v[86:87], v[142:143] op_sel:[1,0]
	v_pk_mul_f32 v[100:101], v[116:117], v[142:143] op_sel_hi:[0,1]
	v_pk_mul_f32 v[120:121], v[116:117], v[142:143] op_sel:[1,0]
	v_pk_fma_f32 v[88:89], v[116:117], v[146:147], v[88:89] op_sel_hi:[0,1,1]
	v_pk_fma_f32 v[100:101], v[118:119], v[146:147], v[100:101] op_sel_hi:[0,1,1]
	v_pk_fma_f32 v[120:121], v[118:119], v[146:147], v[120:121] op_sel:[1,0,0]
	v_pk_fma_f32 v[88:89], v[116:117], v[150:151], v[88:89] op_sel:[1,0,0]
	v_pk_fma_f32 v[100:101], v[118:119], v[150:151], v[100:101] op_sel:[1,0,0]
	v_pk_fma_f32 v[120:121], v[124:125], v[150:151], v[120:121] op_sel_hi:[0,1,1]
	v_pk_mul_f32 v[50:51], v[84:85], v[88:89] op_sel_hi:[0,1]
	v_pk_fma_f32 v[50:51], v[84:85], v[100:101], v[50:51] op_sel:[1,0,0]
	v_pk_fma_f32 v[50:51], v[86:87], v[120:121], v[50:51] op_sel_hi:[0,1,1]
	v_pk_fma_f32 v[50:51], v[124:125], v[96:97], v[50:51] op_sel:[1,0,0] neg_lo:[0,0,1] neg_hi:[0,0,1]
	v_cmp_eq_u32_e64 s[10:11], 6, v127
	v_cmp_eq_u32_e64 s[14:15], 7, v127
	v_pk_add_f32 v[96:97], v[52:53], v[88:89]
	v_pk_add_f32 v[140:141], v[94:95], v[96:97]
	v_pk_add_f32 v[52:53], v[60:61], v[100:101]
	v_pk_add_f32 v[94:95], v[98:99], v[52:53]
	v_pk_add_f32 v[60:61], v[72:73], v[120:121]
	v_pk_add_f32 v[98:99], v[102:103], v[60:61]
	v_pk_add_f32 v[102:103], v[90:91], v[50:51]
	v_pk_add_f32 v[72:73], v[68:69], v[102:103]
	v_pk_fma_f32 v[68:69], v[108:109], v[140:141], v[72:73] op_sel_hi:[0,1,1]
	v_pk_fma_f32 v[144:145], v[112:113], v[140:141], v[72:73] op_sel_hi:[0,1,1]
	v_pk_fma_f32 v[68:69], v[108:109], v[94:95], v[68:69] op_sel:[1,0,0]
	v_pk_fma_f32 v[144:145], v[112:113], v[94:95], v[144:145] op_sel:[1,0,0]
	v_pk_fma_f32 v[68:69], v[110:111], v[98:99], v[68:69] op_sel_hi:[0,1,1]
	v_pk_fma_f32 v[144:145], v[114:115], v[98:99], v[144:145] op_sel_hi:[0,1,1]
	v_pk_fma_f32 v[72:73], v[32:33], v[140:141], v[72:73] op_sel_hi:[0,1,1]
	v_pk_fma_f32 v[72:73], v[32:33], v[94:95], v[72:73] op_sel:[1,0,0]
	v_pk_fma_f32 v[72:73], v[34:35], v[98:99], v[72:73] op_sel_hi:[0,1,1]
	v_cndmask_b32_e64 v90, 0, v18, s[10:11]
	v_cndmask_b32_e64 v91, 0, v18, s[14:15]
	v_add_f32_dpp v72, v68, v72 wave_shl:1 row_mask:0xf bank_mask:0xf bound_ctrl:1
	v_add_f32_dpp v73, v69, v73 wave_shl:1 row_mask:0xf bank_mask:0xf bound_ctrl:1
	s_add_i32 s4, s34, 0
	s_cmpk_lt_i32 s4, 0x201
	s_cselect_b64 s[12:13], s[0:1], 0
	v_add_f32_dpp v72, v144, v72 wave_shr:1 row_mask:0xf bank_mask:0xf bound_ctrl:1
	v_add_f32_dpp v73, v145, v73 wave_shr:1 row_mask:0xf bank_mask:0xf bound_ctrl:1
	v_pk_fma_f32 v[72:73], v[20:21], v[126:127], v[72:73] op_sel_hi:[1,0,1] neg_lo:[0,0,1] neg_hi:[0,0,1]
	v_pk_add_f32 v[72:73], v[72:73], v[90:91] neg_lo:[0,1] neg_hi:[0,1]
	v_pk_mul_f32 v[142:143], v[72:73], v[72:73]
	v_add_f32_e32 v142, v142, v143
	v_cndmask_b32_e64 v143, 0, v142, s[12:13]
	v_add_f32_e32 v1, v1, v143
	s_waitcnt vmcnt(8)
	v_pk_add_f32 v[20:21], v[152:153], v[168:169]
	v_pk_mul_f32 v[32:33], v[152:153], v[152:153] op_sel_hi:[0,1]
	v_pk_mul_f32 v[34:35], v[152:153], v[154:155] op_sel_hi:[1,0]
	v_mul_f32_e64 v68, v153, v153
	v_mul_f32_e64 v69, v154, v154
	v_add_f32_e64 v72, v154, v170
	v_pk_add_f32 v[20:21], v[20:21], v[172:173]
	v_or3_b32 v29, v56, v45, v57
	v_or3_b32 v29, v29, v58, v59
	s_add_i32 s4, s34, 1
	s_cmpk_lt_u32 s4, 0x1ff
	s_cselect_b64 s[12:13], s[42:43], 0
	v_cmp_ne_u32_e64 s[30:31], 0, v29
	s_and_b64 s[30:31], s[30:31], s[12:13]
	v_cndmask_b32_e64 v29, 0, 1.0, s[30:31]
	v_pk_fma_f32 v[32:33], v[168:169], v[168:169], v[32:33] op_sel_hi:[0,1,1]
	v_pk_fma_f32 v[34:35], v[168:169], v[170:171], v[34:35] op_sel_hi:[1,0,1]
	v_fma_f32 v68, v169, v169, v68
	v_fma_f32 v69, v170, v170, v69
	v_add_f32_dpp v73, v29, v29 wave_shr:1 row_mask:0xf bank_mask:0xf bound_ctrl:1
	v_add_f32_e64 v72, v72, v174
	v_pk_fma_f32 v[32:33], v[172:173], v[172:173], v[32:33] op_sel_hi:[0,1,1]
	v_pk_fma_f32 v[34:35], v[172:173], v[174:175], v[34:35] op_sel_hi:[1,0,1]
	v_fma_f32 v68, v173, v173, v68
	v_fma_f32 v69, v174, v174, v69
	v_add_f32_dpp v73, v29, v73 wave_shl:1 row_mask:0xf bank_mask:0xf bound_ctrl:1
	v_pk_add_f32 v[84:85], v[66:67], v[20:21]
	v_pk_add_f32 v[66:67], v[70:71], v[32:33]
	v_pk_add_f32 v[70:71], v[74:75], v[34:35]
	v_pk_add_f32 v[74:75], v[80:81], v[68:69]
	v_pk_add_f32 v[80:81], v[82:83], v[72:73]
	v_mul_f32_e64 v108, v84, v22
	v_mul_f32_e64 v109, v85, v22
	v_mul_f32_e64 v110, v80, v22
	v_fma_f32 v29, v66, v22, v26
	v_mul_f32_e64 v44, v67, v22
	v_mul_f32_e64 v82, v70, v22
	v_fma_f32 v83, v74, v22, v26
	v_mul_f32_e64 v86, v71, v22
	v_fma_f32 v87, v75, v22, v26
	v_fma_f32 v29, -v108, v108, v29
	v_fma_f32 v44, -v108, v109, v44
	v_fma_f32 v82, -v108, v110, v82
	v_fma_f32 v83, -v109, v109, v83
	v_fma_f32 v86, -v109, v110, v86
	v_fma_f32 v87, -v110, v110, v87
	v_mul_f32_e64 v90, v86, v86
	v_mul_f32_e64 v91, v44, v87
	v_mul_f32_e64 v94, v82, v83
	v_mul_f32_e64 v95, v82, v82
	v_mul_f32_e64 v98, v29, v86
	v_mul_f32_e64 v99, v44, v44
	v_fma_f32 v90, v83, v87, -v90
	v_fma_f32 v91, v82, v86, -v91
	v_fma_f32 v94, v44, v86, -v94
	v_fma_f32 v95, v29, v87, -v95
	v_fma_f32 v98, v44, v82, -v98
	v_fma_f32 v99, v29, v83, -v99
	v_mul_f32_e64 v124, v29, v90
	v_fma_f32 v124, v44, v91, v124
	v_fma_f32 v124, v82, v94, v124
	v_rcp_f32_e32 v124, v124
	v_cmp_ne_u32_e64 vcc, s37, v17
	v_mul_f32_e64 v124, v124, v22
	v_cndmask_b32_e64 v124, 0, v124, s[30:31]
	v_cndmask_b32_e64 v29, 0, v18, vcc
	v_cndmask_b32_e64 v117, 0, v22, s[30:31]
	v_mul_f32_e64 v111, v90, v124
	v_mul_f32_e64 v112, v91, v124
	v_mul_f32_e64 v113, v94, v124
	v_mul_f32_e64 v114, v95, v124
	v_mul_f32_e64 v115, v98, v124
	v_mul_f32_e64 v116, v99, v124
	v_add_f32_e64 v118, v81, v29
	v_mov_b32_e32 v119, v17
	ds_write_b128 v23, v[108:111] offset:3072
	ds_write_b128 v23, v[112:115] offset:4096
	ds_write_b128 v23, v[116:119] offset:5120
	v_mov_b32_dpp v80, v54 wave_shr:1 row_mask:0xf bank_mask:0xf bound_ctrl:1
	v_mov_b32_dpp v81, v55 wave_shr:1 row_mask:0xf bank_mask:0xf bound_ctrl:1
	v_mov_b32_dpp v84, v54 wave_shl:1 row_mask:0xf bank_mask:0xf bound_ctrl:1
	v_mov_b32_dpp v85, v55 wave_shl:1 row_mask:0xf bank_mask:0xf bound_ctrl:1
	v_pk_mul_f32 v[66:67], v[54:55], v[152:153] op_sel_hi:[1,0]
	v_pk_mul_f32 v[70:71], v[54:55], v[152:153] op_sel:[0,1]
	v_pk_mul_f32 v[74:75], v[54:55], v[154:155] op_sel_hi:[1,0]
	v_pk_add_f32 v[82:83], v[54:55], v[80:81]
	v_pk_fma_f32 v[66:67], v[80:81], v[168:169], v[66:67] op_sel_hi:[1,0,1]
	v_pk_fma_f32 v[70:71], v[80:81], v[168:169], v[70:71] op_sel:[0,1,0]
	v_pk_fma_f32 v[74:75], v[80:81], v[170:171], v[74:75] op_sel_hi:[1,0,1]
	v_pk_add_f32 v[82:83], v[82:83], v[84:85]
	v_pk_fma_f32 v[66:67], v[84:85], v[172:173], v[66:67] op_sel_hi:[1,0,1]
	v_pk_fma_f32 v[70:71], v[84:85], v[172:173], v[70:71] op_sel:[0,1,0]
	v_pk_fma_f32 v[74:75], v[84:85], v[174:175], v[74:75] op_sel_hi:[1,0,1]
	s_waitcnt lgkmcnt(0)
	s_barrier
	s_add_i32 s5, s34, 6
	s_min_i32 s5, s5, 0x200
	s_mul_i32 s6, s5, 0x804
	s_add_i32 s6, s6, s35
	s_add_i32 s7, s6, 0x505014
	s_add_i32 s8, s6, 0x606018
	s_mul_i32 s9, s5, 0x180c
	s_add_i32 s9, s9, s33
	s_add_i32 s4, s34, 7
	s_min_i32 s4, s4, 0x200
	s_mul_i32 s4, s4, 0x804
	s_add_i32 s4, s4, s38
	buffer_load_dword v17, v28, s[20:23], s4 offen nt
	buffer_load_dwordx3 v[84:86], v27, s[24:27], s9 offen nt
	buffer_load_dword v80, v28, s[16:19], s7 offen nt
	buffer_load_dword v81, v28, s[16:19], s8 offen nt
	s_waitcnt vmcnt(8)
	s_add_i32 s4, s34, 5
	s_cmpk_lt_u32 s4, 0x201
	s_cselect_b64 s[12:13], s[40:41], 0
	v_cmp_eq_u32_e64 s[14:15], s37, v3
	s_and_b64 s[14:15], s[14:15], s[12:13]
	v_cndmask_b32_e64 v29, 0, 1, s[14:15]
	v_mov_b32_dpp v124, v132 wave_shr:1 row_mask:0xf bank_mask:0xf bound_ctrl:1
	v_mov_b32_dpp v125, v133 wave_shr:1 row_mask:0xf bank_mask:0xf bound_ctrl:1
	v_or_b32_dpp v44, v29, v29 wave_shr:1 row_mask:0xf bank_mask:0xf bound_ctrl:1
	v_mov_b32_dpp v126, v134 wave_shr:1 row_mask:0xf bank_mask:0xf bound_ctrl:1
	v_or_b32_dpp v44, v29, v44 wave_shl:1 row_mask:0xf bank_mask:0xf bound_ctrl:1
	v_mov_b32_dpp v140, v132 wave_shl:1 row_mask:0xf bank_mask:0xf bound_ctrl:1
	v_mov_b32_dpp v141, v133 wave_shl:1 row_mask:0xf bank_mask:0xf bound_ctrl:1
	v_or_b32_dpp v59, v44, v44 wave_shr:1 row_mask:0xf bank_mask:0xf bound_ctrl:1
	v_mov_b32_dpp v142, v134 wave_shl:1 row_mask:0xf bank_mask:0xf bound_ctrl:1
	v_or_b32_dpp v59, v44, v59 wave_shl:1 row_mask:0xf bank_mask:0xf bound_ctrl:1
	v_pk_add_f32 v[90:91], v[42:43], v[82:83]
	v_pk_add_f32 v[144:145], v[122:123], v[66:67]
	v_pk_add_f32 v[148:149], v[38:39], v[70:71]
	v_pk_add_f32 v[176:177], v[46:47], v[74:75]
	v_pk_fma_f32 v[144:145], v[108:109], v[90:91], v[144:145] op_sel_hi:[0,1,1] neg_lo:[1,0,0] neg_hi:[1,0,0]
	v_pk_fma_f32 v[148:149], v[108:109], v[90:91], v[148:149] op_sel:[1,0,0] neg_lo:[1,0,0] neg_hi:[1,0,0]
	v_pk_fma_f32 v[176:177], v[110:111], v[90:91], v[176:177] op_sel_hi:[0,1,1] neg_lo:[1,0,0] neg_hi:[1,0,0]
	v_pk_mul_f32 v[38:39], v[110:111], v[144:145] op_sel:[1,0]
	v_pk_mul_f32 v[42:43], v[112:113], v[144:145] op_sel_hi:[0,1]
	v_pk_mul_f32 v[46:47], v[112:113], v[144:145] op_sel:[1,0]
	v_pk_fma_f32 v[38:39], v[112:113], v[148:149], v[38:39] op_sel_hi:[0,1,1]
	v_pk_fma_f32 v[42:43], v[114:115], v[148:149], v[42:43] op_sel_hi:[0,1,1]
	v_pk_fma_f32 v[46:47], v[114:115], v[148:149], v[46:47] op_sel:[1,0,0]
	v_pk_fma_f32 v[38:39], v[112:113], v[176:177], v[38:39] op_sel:[1,0,0]
	v_pk_fma_f32 v[42:43], v[114:115], v[176:177], v[42:43] op_sel:[1,0,0]
	v_pk_fma_f32 v[46:47], v[116:117], v[176:177], v[46:47] op_sel_hi:[0,1,1]
	v_pk_mul_f32 v[180:181], v[108:109], v[38:39] op_sel_hi:[0,1]
	v_pk_fma_f32 v[180:181], v[108:109], v[42:43], v[180:181] op_sel:[1,0,0]
	v_pk_fma_f32 v[180:181], v[110:111], v[46:47], v[180:181] op_sel_hi:[0,1,1]
	v_pk_fma_f32 v[180:181], v[116:117], v[90:91], v[180:181] op_sel:[1,0,0] neg_lo:[0,0,1] neg_hi:[0,0,1]
	v_cmp_eq_u32_e64 s[10:11], 6, v119
	v_cmp_eq_u32_e64 s[14:15], 7, v119
	v_pk_add_f32 v[90:91], v[96:97], v[38:39]
	v_pk_add_f32 v[94:95], v[52:53], v[42:43]
	v_pk_add_f32 v[52:53], v[60:61], v[46:47]
	v_pk_add_f32 v[60:61], v[102:103], v[180:181]
	v_pk_fma_f32 v[96:97], v[156:157], v[90:91], v[60:61] op_sel_hi:[0,1,1]
	v_pk_fma_f32 v[144:145], v[160:161], v[90:91], v[60:61] op_sel_hi:[0,1,1]
	v_pk_fma_f32 v[96:97], v[156:157], v[94:95], v[96:97] op_sel:[1,0,0]
	v_pk_fma_f32 v[144:145], v[160:161], v[94:95], v[144:145] op_sel:[1,0,0]
	v_pk_fma_f32 v[96:97], v[158:159], v[52:53], v[96:97] op_sel_hi:[0,1,1]
	v_pk_fma_f32 v[144:145], v[162:163], v[52:53], v[144:145] op_sel_hi:[0,1,1]
	v_pk_fma_f32 v[60:61], v[76:77], v[90:91], v[60:61] op_sel_hi:[0,1,1]
	v_pk_fma_f32 v[60:61], v[76:77], v[94:95], v[60:61] op_sel:[1,0,0]
	v_pk_fma_f32 v[60:61], v[78:79], v[52:53], v[60:61] op_sel_hi:[0,1,1]
	v_cndmask_b32_e64 v98, 0, v18, s[10:11]
	v_cndmask_b32_e64 v99, 0, v18, s[14:15]
	v_add_f32_dpp v60, v96, v60 wave_shl:1 row_mask:0xf bank_mask:0xf bound_ctrl:1
	v_add_f32_dpp v61, v97, v61 wave_shl:1 row_mask:0xf bank_mask:0xf bound_ctrl:1
	s_add_i32 s4, s34, 1
	s_cmpk_lt_i32 s4, 0x201
	s_cselect_b64 s[12:13], s[0:1], 0
	v_add_f32_dpp v60, v144, v60 wave_shr:1 row_mask:0xf bank_mask:0xf bound_ctrl:1
	v_add_f32_dpp v61, v145, v61 wave_shr:1 row_mask:0xf bank_mask:0xf bound_ctrl:1
	v_pk_fma_f32 v[60:61], v[30:31], v[118:119], v[60:61] op_sel_hi:[1,0,1] neg_lo:[0,0,1] neg_hi:[0,0,1]
	v_pk_add_f32 v[60:61], v[60:61], v[98:99] neg_lo:[0,1] neg_hi:[0,1]
	v_pk_mul_f32 v[102:103], v[60:61], v[60:61]
	v_add_f32_e32 v102, v102, v103
	v_cndmask_b32_e64 v103, 0, v102, s[12:13]
	v_add_f32_e32 v1, v1, v103
	s_waitcnt vmcnt(8)
	v_pk_add_f32 v[30:31], v[132:133], v[124:125]
	v_pk_mul_f32 v[52:53], v[132:133], v[132:133] op_sel_hi:[0,1]
	v_pk_mul_f32 v[60:61], v[132:133], v[134:135] op_sel_hi:[1,0]
	v_mul_f32_e64 v76, v133, v133
	v_mul_f32_e64 v77, v134, v134
	v_add_f32_e64 v78, v134, v126
	v_pk_add_f32 v[30:31], v[30:31], v[140:141]
	v_or3_b32 v29, v59, v56, v45
	v_or3_b32 v29, v29, v57, v58
	s_add_i32 s4, s34, 2
	s_cmpk_lt_u32 s4, 0x1ff
	s_cselect_b64 s[12:13], s[42:43], 0
	v_cmp_ne_u32_e64 s[30:31], 0, v29
	s_and_b64 s[30:31], s[30:31], s[12:13]
	v_cndmask_b32_e64 v29, 0, 1.0, s[30:31]
	v_pk_fma_f32 v[52:53], v[124:125], v[124:125], v[52:53] op_sel_hi:[0,1,1]
	v_pk_fma_f32 v[60:61], v[124:125], v[126:127], v[60:61] op_sel_hi:[1,0,1]
	v_fma_f32 v76, v125, v125, v76
	v_fma_f32 v77, v126, v126, v77
	v_add_f32_dpp v79, v29, v29 wave_shr:1 row_mask:0xf bank_mask:0xf bound_ctrl:1
	v_add_f32_e64 v78, v78, v142
	v_pk_fma_f32 v[52:53], v[140:141], v[140:141], v[52:53] op_sel_hi:[0,1,1]
	v_pk_fma_f32 v[60:61], v[140:141], v[142:143], v[60:61] op_sel_hi:[1,0,1]
	v_fma_f32 v76, v141, v141, v76
	v_fma_f32 v77, v142, v142, v77
	v_add_f32_dpp v79, v29, v79 wave_shl:1 row_mask:0xf bank_mask:0xf bound_ctrl:1
	v_pk_add_f32 v[96:97], v[20:21], v[30:31]
	v_pk_add_f32 v[90:91], v[6:7], v[96:97]
	v_pk_add_f32 v[6:7], v[32:33], v[52:53]
	v_pk_add_f32 v[20:21], v[12:13], v[6:7]
	v_pk_add_f32 v[12:13], v[34:35], v[60:61]
	v_pk_add_f32 v[32:33], v[14:15], v[12:13]
	v_pk_add_f32 v[14:15], v[68:69], v[76:77]
	v_pk_add_f32 v[34:35], v[48:49], v[14:15]
	v_pk_add_f32 v[48:49], v[72:73], v[78:79]
	v_pk_add_f32 v[68:69], v[62:63], v[48:49]
	v_mul_f32_e64 v108, v90, v22
	v_mul_f32_e64 v109, v91, v22
	v_mul_f32_e64 v110, v68, v22
	v_fma_f32 v29, v20, v22, v26
	v_mul_f32_e64 v44, v21, v22
	v_mul_f32_e64 v62, v32, v22
	v_fma_f32 v63, v34, v22, v26
	v_mul_f32_e64 v72, v33, v22
	v_fma_f32 v73, v35, v22, v26
	v_fma_f32 v29, -v108, v108, v29
	v_fma_f32 v44, -v108, v109, v44
	v_fma_f32 v62, -v108, v110, v62
	v_fma_f32 v63, -v109, v109, v63
	v_fma_f32 v72, -v109, v110, v72
	v_fma_f32 v73, -v110, v110, v73
	v_mul_f32_e64 v94, v72, v72
	v_mul_f32_e64 v95, v44, v73
	v_mul_f32_e64 v98, v62, v63
	v_mul_f32_e64 v99, v62, v62
	v_mul_f32_e64 v102, v29, v72
	v_mul_f32_e64 v103, v44, v44
	v_fma_f32 v94, v63, v73, -v94
	v_fma_f32 v95, v62, v72, -v95
	v_fma_f32 v98, v44, v72, -v98
	v_fma_f32 v99, v29, v73, -v99
	v_fma_f32 v102, v44, v62, -v102
	v_fma_f32 v103, v29, v63, -v103
	v_mul_f32_e64 v122, v29, v94
	v_fma_f32 v122, v44, v95, v122
	v_fma_f32 v122, v62, v98, v122
	v_rcp_f32_e32 v122, v122
	v_cmp_ne_u32_e64 vcc, s37, v25
	v_mul_f32_e64 v122, v122, v22
	v_cndmask_b32_e64 v122, 0, v122, s[30:31]
	v_cndmask_b32_e64 v29, 0, v18, vcc
	v_cndmask_b32_e64 v117, 0, v22, s[30:31]
	v_mul_f32_e64 v111, v94, v122
	v_mul_f32_e64 v112, v95, v122
	v_mul_f32_e64 v113, v98, v122
	v_mul_f32_e64 v114, v99, v122
	v_mul_f32_e64 v115, v102, v122
	v_mul_f32_e64 v116, v103, v122
	v_add_f32_e64 v118, v69, v29
	v_mov_b32_e32 v119, v25
	ds_write_b128 v23, v[108:111]
	ds_write_b128 v23, v[112:115] offset:1024
	ds_write_b128 v23, v[116:119] offset:2048
	v_mov_b32_dpp v34, v36 wave_shr:1 row_mask:0xf bank_mask:0xf bound_ctrl:1
	v_mov_b32_dpp v35, v37 wave_shr:1 row_mask:0xf bank_mask:0xf bound_ctrl:1
	v_mov_b32_dpp v62, v36 wave_shl:1 row_mask:0xf bank_mask:0xf bound_ctrl:1
	v_mov_b32_dpp v63, v37 wave_shl:1 row_mask:0xf bank_mask:0xf bound_ctrl:1
	v_pk_mul_f32 v[20:21], v[36:37], v[132:133] op_sel_hi:[1,0]
	v_pk_mul_f32 v[32:33], v[36:37], v[132:133] op_sel:[0,1]
	v_pk_mul_f32 v[68:69], v[36:37], v[134:135] op_sel_hi:[1,0]
	v_pk_add_f32 v[72:73], v[36:37], v[34:35]
	v_pk_fma_f32 v[20:21], v[34:35], v[124:125], v[20:21] op_sel_hi:[1,0,1]
	v_pk_fma_f32 v[32:33], v[34:35], v[124:125], v[32:33] op_sel:[0,1,0]
	v_pk_fma_f32 v[68:69], v[34:35], v[126:127], v[68:69] op_sel_hi:[1,0,1]
	v_pk_add_f32 v[72:73], v[72:73], v[62:63]
	v_pk_fma_f32 v[20:21], v[62:63], v[140:141], v[20:21] op_sel_hi:[1,0,1]
	v_pk_fma_f32 v[32:33], v[62:63], v[140:141], v[32:33] op_sel:[0,1,0]
	v_pk_fma_f32 v[68:69], v[62:63], v[142:143], v[68:69] op_sel_hi:[1,0,1]
	s_waitcnt lgkmcnt(0)
	s_barrier
	s_add_i32 s5, s34, 7
	s_min_i32 s5, s5, 0x200
	s_mul_i32 s6, s5, 0x804
	s_add_i32 s6, s6, s35
	s_add_i32 s7, s6, 0x505014
	s_add_i32 s8, s6, 0x606018
	s_mul_i32 s9, s5, 0x180c
	s_add_i32 s9, s9, s33
	s_add_i32 s4, s34, 8
	s_min_i32 s4, s4, 0x200
	s_mul_i32 s4, s4, 0x804
	s_add_i32 s4, s4, s38
	buffer_load_dword v25, v28, s[20:23], s4 offen nt
	buffer_load_dwordx3 v[144:146], v27, s[24:27], s9 offen nt
	buffer_load_dword v34, v28, s[16:19], s7 offen nt
	buffer_load_dword v35, v28, s[16:19], s8 offen nt
	s_waitcnt vmcnt(8)
	s_add_i32 s4, s34, 6
	s_cmpk_lt_u32 s4, 0x201
	s_cselect_b64 s[12:13], s[40:41], 0
	v_cmp_eq_u32_e64 s[14:15], s37, v16
	s_and_b64 s[14:15], s[14:15], s[12:13]
	v_cndmask_b32_e64 v29, 0, 1, s[14:15]
	v_mov_b32_dpp v148, v128 wave_shr:1 row_mask:0xf bank_mask:0xf bound_ctrl:1
	v_mov_b32_dpp v149, v129 wave_shr:1 row_mask:0xf bank_mask:0xf bound_ctrl:1
	v_or_b32_dpp v44, v29, v29 wave_shr:1 row_mask:0xf bank_mask:0xf bound_ctrl:1
	v_mov_b32_dpp v150, v130 wave_shr:1 row_mask:0xf bank_mask:0xf bound_ctrl:1
	v_or_b32_dpp v44, v29, v44 wave_shl:1 row_mask:0xf bank_mask:0xf bound_ctrl:1
	v_mov_b32_dpp v156, v128 wave_shl:1 row_mask:0xf bank_mask:0xf bound_ctrl:1
	v_mov_b32_dpp v157, v129 wave_shl:1 row_mask:0xf bank_mask:0xf bound_ctrl:1
	v_or_b32_dpp v58, v44, v44 wave_shr:1 row_mask:0xf bank_mask:0xf bound_ctrl:1
	v_mov_b32_dpp v158, v130 wave_shl:1 row_mask:0xf bank_mask:0xf bound_ctrl:1
	v_or_b32_dpp v58, v44, v58 wave_shl:1 row_mask:0xf bank_mask:0xf bound_ctrl:1
	v_pk_add_f32 v[62:63], v[82:83], v[72:73]
	v_pk_add_f32 v[90:91], v[64:65], v[62:63]
	v_pk_add_f32 v[82:83], v[66:67], v[20:21]
	v_pk_add_f32 v[64:65], v[4:5], v[82:83]
	v_pk_add_f32 v[66:67], v[70:71], v[32:33]
	v_pk_add_f32 v[4:5], v[8:9], v[66:67]
	v_pk_add_f32 v[70:71], v[74:75], v[68:69]
	v_pk_add_f32 v[8:9], v[40:41], v[70:71]
	v_pk_fma_f32 v[64:65], v[108:109], v[90:91], v[64:65] op_sel_hi:[0,1,1] neg_lo:[1,0,0] neg_hi:[1,0,0]
	v_pk_fma_f32 v[4:5], v[108:109], v[90:91], v[4:5] op_sel:[1,0,0] neg_lo:[1,0,0] neg_hi:[1,0,0]
	v_pk_fma_f32 v[8:9], v[110:111], v[90:91], v[8:9] op_sel_hi:[0,1,1] neg_lo:[1,0,0] neg_hi:[1,0,0]
	v_pk_mul_f32 v[74:75], v[110:111], v[64:65] op_sel:[1,0]
	v_pk_mul_f32 v[94:95], v[112:113], v[64:65] op_sel_hi:[0,1]
	v_pk_mul_f32 v[98:99], v[112:113], v[64:65] op_sel:[1,0]
	v_pk_fma_f32 v[74:75], v[112:113], v[4:5], v[74:75] op_sel_hi:[0,1,1]
	v_pk_fma_f32 v[94:95], v[114:115], v[4:5], v[94:95] op_sel_hi:[0,1,1]
	v_pk_fma_f32 v[98:99], v[114:115], v[4:5], v[98:99] op_sel:[1,0,0]
	v_pk_fma_f32 v[74:75], v[112:113], v[8:9], v[74:75] op_sel:[1,0,0]
	v_pk_fma_f32 v[94:95], v[114:115], v[8:9], v[94:95] op_sel:[1,0,0]
	v_pk_fma_f32 v[98:99], v[116:117], v[8:9], v[98:99] op_sel_hi:[0,1,1]
	v_pk_mul_f32 v[40:41], v[108:109], v[74:75] op_sel_hi:[0,1]
	v_pk_fma_f32 v[40:41], v[108:109], v[94:95], v[40:41] op_sel:[1,0,0]
	v_pk_fma_f32 v[40:41], v[110:111], v[98:99], v[40:41] op_sel_hi:[0,1,1]
	v_pk_fma_f32 v[40:41], v[116:117], v[90:91], v[40:41] op_sel:[1,0,0] neg_lo:[0,0,1] neg_hi:[0,0,1]
	v_cmp_eq_u32_e64 s[10:11], 6, v119
	v_cmp_eq_u32_e64 s[14:15], 7, v119
	v_pk_add_f32 v[90:91], v[38:39], v[74:75]
	v_pk_add_f32 v[4:5], v[88:89], v[90:91]
	v_pk_add_f32 v[38:39], v[42:43], v[94:95]
	v_pk_add_f32 v[8:9], v[100:101], v[38:39]
	v_pk_add_f32 v[42:43], v[46:47], v[98:99]
	v_pk_add_f32 v[64:65], v[120:121], v[42:43]
	v_pk_add_f32 v[88:89], v[180:181], v[40:41]
	v_pk_add_f32 v[46:47], v[50:51], v[88:89]
	v_pk_fma_f32 v[50:51], v[136:137], v[4:5], v[46:47] op_sel_hi:[0,1,1]
	v_pk_fma_f32 v[102:103], v[164:165], v[4:5], v[46:47] op_sel_hi:[0,1,1]
	v_pk_fma_f32 v[50:51], v[136:137], v[8:9], v[50:51] op_sel:[1,0,0]
	v_pk_fma_f32 v[102:103], v[164:165], v[8:9], v[102:103] op_sel:[1,0,0]
	v_pk_fma_f32 v[50:51], v[138:139], v[64:65], v[50:51] op_sel_hi:[0,1,1]
	v_pk_fma_f32 v[102:103], v[166:167], v[64:65], v[102:103] op_sel_hi:[0,1,1]
	v_pk_fma_f32 v[46:47], v[104:105], v[4:5], v[46:47] op_sel_hi:[0,1,1]
	v_pk_fma_f32 v[46:47], v[104:105], v[8:9], v[46:47] op_sel:[1,0,0]
	v_pk_fma_f32 v[46:47], v[106:107], v[64:65], v[46:47] op_sel_hi:[0,1,1]
	v_cndmask_b32_e64 v100, 0, v18, s[10:11]
	v_cndmask_b32_e64 v101, 0, v18, s[14:15]
	v_add_f32_dpp v46, v50, v46 wave_shl:1 row_mask:0xf bank_mask:0xf bound_ctrl:1
	v_add_f32_dpp v47, v51, v47 wave_shl:1 row_mask:0xf bank_mask:0xf bound_ctrl:1
	s_add_i32 s4, s34, 2
	s_cmpk_lt_i32 s4, 0x201
	s_cselect_b64 s[12:13], s[0:1], 0
	v_add_f32_dpp v46, v102, v46 wave_shr:1 row_mask:0xf bank_mask:0xf bound_ctrl:1
	v_add_f32_dpp v47, v103, v47 wave_shr:1 row_mask:0xf bank_mask:0xf bound_ctrl:1
	v_pk_fma_f32 v[46:47], v[92:93], v[118:119], v[46:47] op_sel_hi:[1,0,1] neg_lo:[0,0,1] neg_hi:[0,0,1]
	v_pk_add_f32 v[46:47], v[46:47], v[100:101] neg_lo:[0,1] neg_hi:[0,1]
	v_pk_mul_f32 v[120:121], v[46:47], v[46:47]
	v_add_f32_e32 v120, v120, v121
	v_cndmask_b32_e64 v121, 0, v120, s[12:13]
	v_add_f32_e32 v1, v1, v121
	s_waitcnt vmcnt(8)
	v_pk_add_f32 v[4:5], v[128:129], v[148:149]
	v_pk_mul_f32 v[8:9], v[128:129], v[128:129] op_sel_hi:[0,1]
	v_pk_mul_f32 v[46:47], v[128:129], v[130:131] op_sel_hi:[1,0]
	v_mul_f32_e64 v50, v129, v129
	v_mul_f32_e64 v51, v130, v130
	v_add_f32_e64 v64, v130, v150
	v_pk_add_f32 v[4:5], v[4:5], v[156:157]
	v_or3_b32 v29, v58, v59, v56
	v_or3_b32 v29, v29, v45, v57
	s_add_i32 s4, s34, 3
	s_cmpk_lt_u32 s4, 0x1ff
	s_cselect_b64 s[12:13], s[42:43], 0
	v_cmp_ne_u32_e64 s[30:31], 0, v29
	s_and_b64 s[30:31], s[30:31], s[12:13]
	v_cndmask_b32_e64 v29, 0, 1.0, s[30:31]
	v_pk_fma_f32 v[8:9], v[148:149], v[148:149], v[8:9] op_sel_hi:[0,1,1]
	v_pk_fma_f32 v[46:47], v[148:149], v[150:151], v[46:47] op_sel_hi:[1,0,1]
	v_fma_f32 v50, v149, v149, v50
	v_fma_f32 v51, v150, v150, v51
	v_add_f32_dpp v65, v29, v29 wave_shr:1 row_mask:0xf bank_mask:0xf bound_ctrl:1
	v_add_f32_e64 v64, v64, v158
	v_pk_fma_f32 v[8:9], v[156:157], v[156:157], v[8:9] op_sel_hi:[0,1,1]
	v_pk_fma_f32 v[46:47], v[156:157], v[158:159], v[46:47] op_sel_hi:[1,0,1]
	v_fma_f32 v50, v157, v157, v50
	v_fma_f32 v51, v158, v158, v51
	v_add_f32_dpp v65, v29, v65 wave_shl:1 row_mask:0xf bank_mask:0xf bound_ctrl:1
	v_pk_add_f32 v[92:93], v[96:97], v[4:5]
	v_pk_add_f32 v[96:97], v[6:7], v[8:9]
	v_pk_add_f32 v[6:7], v[12:13], v[46:47]
	v_pk_add_f32 v[12:13], v[14:15], v[50:51]
	v_pk_add_f32 v[14:15], v[48:49], v[64:65]
	v_mul_f32_e64 v100, v92, v22
	v_mul_f32_e64 v101, v93, v22
	v_mul_f32_e64 v102, v14, v22
	v_fma_f32 v29, v96, v22, v26
	v_mul_f32_e64 v44, v97, v22
	v_mul_f32_e64 v48, v6, v22
	v_fma_f32 v49, v12, v22, v26
	v_mul_f32_e64 v112, v7, v22
	v_fma_f32 v113, v13, v22, v26
	v_fma_f32 v29, -v100, v100, v29
	v_fma_f32 v44, -v100, v101, v44
	v_fma_f32 v48, -v100, v102, v48
	v_fma_f32 v49, -v101, v101, v49
	v_fma_f32 v112, -v101, v102, v112
	v_fma_f32 v113, -v102, v102, v113
	v_mul_f32_e64 v114, v112, v112
	v_mul_f32_e64 v115, v44, v113
	v_mul_f32_e64 v116, v48, v49
	v_mul_f32_e64 v117, v48, v48
	v_mul_f32_e64 v118, v29, v112
	v_mul_f32_e64 v119, v44, v44
	v_fma_f32 v114, v49, v113, -v114
	v_fma_f32 v115, v48, v112, -v115
	v_fma_f32 v116, v44, v112, -v116
	v_fma_f32 v117, v29, v113, -v117
	v_fma_f32 v118, v44, v48, -v118
	v_fma_f32 v119, v29, v49, -v119
	v_mul_f32_e64 v120, v29, v114
	v_fma_f32 v120, v44, v115, v120
	v_fma_f32 v120, v48, v116, v120
	v_rcp_f32_e32 v120, v120
	v_cmp_ne_u32_e64 vcc, s37, v24
	v_mul_f32_e64 v120, v120, v22
	v_cndmask_b32_e64 v120, 0, v120, s[30:31]
	v_cndmask_b32_e64 v29, 0, v18, vcc
	v_cndmask_b32_e64 v109, 0, v22, s[30:31]
	v_mul_f32_e64 v103, v114, v120
	v_mul_f32_e64 v104, v115, v120
	v_mul_f32_e64 v105, v116, v120
	v_mul_f32_e64 v106, v117, v120
	v_mul_f32_e64 v107, v118, v120
	v_mul_f32_e64 v108, v119, v120
	v_add_f32_e64 v110, v15, v29
	v_mov_b32_e32 v111, v24
	ds_write_b128 v23, v[100:103] offset:3072
	ds_write_b128 v23, v[104:107] offset:4096
	ds_write_b128 v23, v[108:111] offset:5120
	v_mov_b32_dpp v12, v10 wave_shr:1 row_mask:0xf bank_mask:0xf bound_ctrl:1
	v_mov_b32_dpp v13, v11 wave_shr:1 row_mask:0xf bank_mask:0xf bound_ctrl:1
	v_mov_b32_dpp v48, v10 wave_shl:1 row_mask:0xf bank_mask:0xf bound_ctrl:1
	v_mov_b32_dpp v49, v11 wave_shl:1 row_mask:0xf bank_mask:0xf bound_ctrl:1
	v_pk_mul_f32 v[6:7], v[10:11], v[128:129] op_sel_hi:[1,0]
	v_pk_mul_f32 v[14:15], v[10:11], v[128:129] op_sel:[0,1]
	v_pk_mul_f32 v[114:115], v[10:11], v[130:131] op_sel_hi:[1,0]
	v_pk_add_f32 v[118:119], v[10:11], v[12:13]
	v_pk_fma_f32 v[6:7], v[12:13], v[148:149], v[6:7] op_sel_hi:[1,0,1]
	v_pk_fma_f32 v[14:15], v[12:13], v[148:149], v[14:15] op_sel:[0,1,0]
	v_pk_fma_f32 v[114:115], v[12:13], v[150:151], v[114:115] op_sel_hi:[1,0,1]
	v_pk_add_f32 v[118:119], v[118:119], v[48:49]
	v_pk_fma_f32 v[6:7], v[48:49], v[156:157], v[6:7] op_sel_hi:[1,0,1]
	v_pk_fma_f32 v[14:15], v[48:49], v[156:157], v[14:15] op_sel:[0,1,0]
	v_pk_fma_f32 v[114:115], v[48:49], v[158:159], v[114:115] op_sel_hi:[1,0,1]
	s_waitcnt lgkmcnt(0)
	s_barrier
	s_add_i32 s5, s34, 8
	s_min_i32 s5, s5, 0x200
	s_mul_i32 s6, s5, 0x804
	s_add_i32 s6, s6, s35
	s_add_i32 s7, s6, 0x505014
	s_add_i32 s8, s6, 0x606018
	s_mul_i32 s9, s5, 0x180c
	s_add_i32 s9, s9, s33
	s_add_i32 s4, s34, 9
	s_min_i32 s4, s4, 0x200
	s_mul_i32 s4, s4, 0x804
	s_add_i32 s4, s4, s38
	buffer_load_dword v24, v28, s[20:23], s4 offen nt
	buffer_load_dwordx3 v[120:122], v27, s[24:27], s9 offen nt
	buffer_load_dword v12, v28, s[16:19], s7 offen nt
	buffer_load_dword v13, v28, s[16:19], s8 offen nt
	s_waitcnt vmcnt(8)
	s_add_i32 s4, s34, 7
	s_cmpk_lt_u32 s4, 0x201
	s_cselect_b64 s[12:13], s[40:41], 0
	v_cmp_eq_u32_e64 s[14:15], s37, v17
	s_and_b64 s[14:15], s[14:15], s[12:13]
	v_cndmask_b32_e64 v29, 0, 1, s[14:15]
	v_mov_b32_dpp v136, v84 wave_shr:1 row_mask:0xf bank_mask:0xf bound_ctrl:1
	v_mov_b32_dpp v137, v85 wave_shr:1 row_mask:0xf bank_mask:0xf bound_ctrl:1
	v_or_b32_dpp v44, v29, v29 wave_shr:1 row_mask:0xf bank_mask:0xf bound_ctrl:1
	v_mov_b32_dpp v138, v86 wave_shr:1 row_mask:0xf bank_mask:0xf bound_ctrl:1
	v_or_b32_dpp v44, v29, v44 wave_shl:1 row_mask:0xf bank_mask:0xf bound_ctrl:1
	v_mov_b32_dpp v160, v84 wave_shl:1 row_mask:0xf bank_mask:0xf bound_ctrl:1
	v_mov_b32_dpp v161, v85 wave_shl:1 row_mask:0xf bank_mask:0xf bound_ctrl:1
	v_or_b32_dpp v57, v44, v44 wave_shr:1 row_mask:0xf bank_mask:0xf bound_ctrl:1
	v_mov_b32_dpp v162, v86 wave_shl:1 row_mask:0xf bank_mask:0xf bound_ctrl:1
	v_or_b32_dpp v57, v44, v57 wave_shl:1 row_mask:0xf bank_mask:0xf bound_ctrl:1
	v_pk_add_f32 v[48:49], v[62:63], v[118:119]
	v_pk_add_f32 v[62:63], v[82:83], v[6:7]
	v_pk_add_f32 v[82:83], v[66:67], v[14:15]
	v_pk_add_f32 v[66:67], v[70:71], v[114:115]
	v_pk_fma_f32 v[62:63], v[100:101], v[48:49], v[62:63] op_sel_hi:[0,1,1] neg_lo:[1,0,0] neg_hi:[1,0,0]
	v_pk_fma_f32 v[82:83], v[100:101], v[48:49], v[82:83] op_sel:[1,0,0] neg_lo:[1,0,0] neg_hi:[1,0,0]
	v_pk_fma_f32 v[66:67], v[102:103], v[48:49], v[66:67] op_sel_hi:[0,1,1] neg_lo:[1,0,0] neg_hi:[1,0,0]
	v_pk_mul_f32 v[92:93], v[102:103], v[62:63] op_sel:[1,0]
	v_pk_mul_f32 v[96:97], v[104:105], v[62:63] op_sel_hi:[0,1]
	v_pk_mul_f32 v[112:113], v[104:105], v[62:63] op_sel:[1,0]
	v_pk_fma_f32 v[92:93], v[104:105], v[82:83], v[92:93] op_sel_hi:[0,1,1]
	v_pk_fma_f32 v[96:97], v[106:107], v[82:83], v[96:97] op_sel_hi:[0,1,1]
	v_pk_fma_f32 v[112:113], v[106:107], v[82:83], v[112:113] op_sel:[1,0,0]
	v_pk_fma_f32 v[92:93], v[104:105], v[66:67], v[92:93] op_sel:[1,0,0]
	v_pk_fma_f32 v[96:97], v[106:107], v[66:67], v[96:97] op_sel:[1,0,0]
	v_pk_fma_f32 v[112:113], v[108:109], v[66:67], v[112:113] op_sel_hi:[0,1,1]
	v_pk_mul_f32 v[70:71], v[100:101], v[92:93] op_sel_hi:[0,1]
	v_pk_fma_f32 v[70:71], v[100:101], v[96:97], v[70:71] op_sel:[1,0,0]
	v_pk_fma_f32 v[70:71], v[102:103], v[112:113], v[70:71] op_sel_hi:[0,1,1]
	v_pk_fma_f32 v[70:71], v[108:109], v[48:49], v[70:71] op_sel:[1,0,0] neg_lo:[0,0,1] neg_hi:[0,0,1]
	v_cmp_eq_u32_e64 s[10:11], 6, v111
	v_cmp_eq_u32_e64 s[14:15], 7, v111
	v_pk_add_f32 v[48:49], v[90:91], v[92:93]
	v_pk_add_f32 v[62:63], v[38:39], v[96:97]
	v_pk_add_f32 v[38:39], v[42:43], v[112:113]
	v_pk_add_f32 v[116:117], v[88:89], v[70:71]
	v_pk_fma_f32 v[88:89], v[168:169], v[48:49], v[116:117] op_sel_hi:[0,1,1]
	v_pk_fma_f32 v[164:165], v[172:173], v[48:49], v[116:117] op_sel_hi:[0,1,1]
	v_pk_fma_f32 v[88:89], v[168:169], v[62:63], v[88:89] op_sel:[1,0,0]
	v_pk_fma_f32 v[164:165], v[172:173], v[62:63], v[164:165] op_sel:[1,0,0]
	v_pk_fma_f32 v[88:89], v[170:171], v[38:39], v[88:89] op_sel_hi:[0,1,1]
	v_pk_fma_f32 v[164:165], v[174:175], v[38:39], v[164:165] op_sel_hi:[0,1,1]
	v_pk_fma_f32 v[116:117], v[152:153], v[48:49], v[116:117] op_sel_hi:[0,1,1]
	v_pk_fma_f32 v[116:117], v[152:153], v[62:63], v[116:117] op_sel:[1,0,0]
	v_pk_fma_f32 v[116:117], v[154:155], v[38:39], v[116:117] op_sel_hi:[0,1,1]
	v_cndmask_b32_e64 v42, 0, v18, s[10:11]
	v_cndmask_b32_e64 v43, 0, v18, s[14:15]
	v_add_f32_dpp v116, v88, v116 wave_shl:1 row_mask:0xf bank_mask:0xf bound_ctrl:1
	v_add_f32_dpp v117, v89, v117 wave_shl:1 row_mask:0xf bank_mask:0xf bound_ctrl:1
	s_add_i32 s4, s34, 3
	s_cmpk_lt_i32 s4, 0x201
	s_cselect_b64 s[12:13], s[0:1], 0
	v_add_f32_dpp v116, v164, v116 wave_shr:1 row_mask:0xf bank_mask:0xf bound_ctrl:1
	v_add_f32_dpp v117, v165, v117 wave_shr:1 row_mask:0xf bank_mask:0xf bound_ctrl:1
	v_pk_fma_f32 v[116:117], v[54:55], v[110:111], v[116:117] op_sel_hi:[1,0,1] neg_lo:[0,0,1] neg_hi:[0,0,1]
	v_pk_add_f32 v[116:117], v[116:117], v[42:43] neg_lo:[0,1] neg_hi:[0,1]
	v_pk_mul_f32 v[66:67], v[116:117], v[116:117]
	v_add_f32_e32 v66, v66, v67
	v_cndmask_b32_e64 v67, 0, v66, s[12:13]
	v_add_f32_e32 v1, v1, v67
	s_waitcnt vmcnt(8)
	v_pk_add_f32 v[38:39], v[84:85], v[136:137]
	v_pk_mul_f32 v[42:43], v[84:85], v[84:85] op_sel_hi:[0,1]
	v_pk_mul_f32 v[48:49], v[84:85], v[86:87] op_sel_hi:[1,0]
	v_mul_f32_e64 v54, v85, v85
	v_mul_f32_e64 v55, v86, v86
	v_add_f32_e64 v62, v86, v138
	v_pk_add_f32 v[38:39], v[38:39], v[160:161]
	v_or3_b32 v29, v57, v58, v59
	v_or3_b32 v29, v29, v56, v45
	s_add_i32 s4, s34, 4
	s_cmpk_lt_u32 s4, 0x1ff
	s_cselect_b64 s[12:13], s[42:43], 0
	v_cmp_ne_u32_e64 s[30:31], 0, v29
	s_and_b64 s[30:31], s[30:31], s[12:13]
	v_cndmask_b32_e64 v29, 0, 1.0, s[30:31]
	v_pk_fma_f32 v[42:43], v[136:137], v[136:137], v[42:43] op_sel_hi:[0,1,1]
	v_pk_fma_f32 v[48:49], v[136:137], v[138:139], v[48:49] op_sel_hi:[1,0,1]
	v_fma_f32 v54, v137, v137, v54
	v_fma_f32 v55, v138, v138, v55
	v_add_f32_dpp v63, v29, v29 wave_shr:1 row_mask:0xf bank_mask:0xf bound_ctrl:1
	v_add_f32_e64 v62, v62, v162
	v_pk_fma_f32 v[42:43], v[160:161], v[160:161], v[42:43] op_sel_hi:[0,1,1]
	v_pk_fma_f32 v[48:49], v[160:161], v[162:163], v[48:49] op_sel_hi:[1,0,1]
	v_fma_f32 v54, v161, v161, v54
	v_fma_f32 v55, v162, v162, v55
	v_add_f32_dpp v63, v29, v63 wave_shl:1 row_mask:0xf bank_mask:0xf bound_ctrl:1
	v_pk_add_f32 v[88:89], v[4:5], v[38:39]
	v_pk_add_f32 v[66:67], v[30:31], v[88:89]
	v_pk_add_f32 v[30:31], v[8:9], v[42:43]
	v_pk_add_f32 v[4:5], v[52:53], v[30:31]
	v_pk_add_f32 v[82:83], v[46:47], v[48:49]
	v_pk_add_f32 v[8:9], v[60:61], v[82:83]
	v_pk_add_f32 v[46:47], v[50:51], v[54:55]
	v_pk_add_f32 v[52:53], v[76:77], v[46:47]
	v_pk_add_f32 v[60:61], v[64:65], v[62:63]
	v_pk_add_f32 v[50:51], v[78:79], v[60:61]
	v_mul_f32_e64 v76, v66, v22
	v_mul_f32_e64 v77, v67, v22
	v_mul_f32_e64 v78, v50, v22
	v_fma_f32 v29, v4, v22, v26
	v_mul_f32_e64 v44, v5, v22
	v_mul_f32_e64 v64, v8, v22
	v_fma_f32 v65, v52, v22, v26
	v_mul_f32_e64 v90, v9, v22
	v_fma_f32 v91, v53, v22, v26
	v_fma_f32 v29, -v76, v76, v29
	v_fma_f32 v44, -v76, v77, v44
	v_fma_f32 v64, -v76, v78, v64
	v_fma_f32 v65, -v77, v77, v65
	v_fma_f32 v90, -v77, v78, v90
	v_fma_f32 v91, -v78, v78, v91
	v_mul_f32_e64 v108, v90, v90
	v_mul_f32_e64 v109, v44, v91
	v_mul_f32_e64 v110, v64, v65
	v_mul_f32_e64 v111, v64, v64
	v_mul_f32_e64 v116, v29, v90
	v_mul_f32_e64 v117, v44, v44
	v_fma_f32 v108, v65, v91, -v108
	v_fma_f32 v109, v64, v90, -v109
	v_fma_f32 v110, v44, v90, -v110
	v_fma_f32 v111, v29, v91, -v111
	v_fma_f32 v116, v44, v64, -v116
	v_fma_f32 v117, v29, v65, -v117
	v_mul_f32_e64 v152, v29, v108
	v_fma_f32 v152, v44, v109, v152
	v_fma_f32 v152, v64, v110, v152
	v_rcp_f32_e32 v152, v152
	v_cmp_ne_u32_e64 vcc, s37, v2
	v_mul_f32_e64 v152, v152, v22
	v_cndmask_b32_e64 v152, 0, v152, s[30:31]
	v_cndmask_b32_e64 v29, 0, v18, vcc
	v_cndmask_b32_e64 v105, 0, v22, s[30:31]
	v_mul_f32_e64 v79, v108, v152
	v_mul_f32_e64 v100, v109, v152
	v_mul_f32_e64 v101, v110, v152
	v_mul_f32_e64 v102, v111, v152
	v_mul_f32_e64 v103, v116, v152
	v_mul_f32_e64 v104, v117, v152
	v_add_f32_e64 v106, v51, v29
	v_mov_b32_e32 v107, v2
	ds_write_b128 v23, v[76:79]
	ds_write_b128 v23, v[100:103] offset:1024
	ds_write_b128 v23, v[104:107] offset:2048
	v_mov_b32_dpp v50, v80 wave_shr:1 row_mask:0xf bank_mask:0xf bound_ctrl:1
	v_mov_b32_dpp v51, v81 wave_shr:1 row_mask:0xf bank_mask:0xf bound_ctrl:1
	v_mov_b32_dpp v66, v80 wave_shl:1 row_mask:0xf bank_mask:0xf bound_ctrl:1
	v_mov_b32_dpp v67, v81 wave_shl:1 row_mask:0xf bank_mask:0xf bound_ctrl:1
	v_pk_mul_f32 v[4:5], v[80:81], v[84:85] op_sel_hi:[1,0]
	v_pk_mul_f32 v[8:9], v[80:81], v[84:85] op_sel:[0,1]
	v_pk_mul_f32 v[44:45], v[80:81], v[86:87] op_sel_hi:[1,0]
	v_pk_add_f32 v[52:53], v[80:81], v[50:51]
	v_pk_fma_f32 v[4:5], v[50:51], v[136:137], v[4:5] op_sel_hi:[1,0,1]
	v_pk_fma_f32 v[8:9], v[50:51], v[136:137], v[8:9] op_sel:[0,1,0]
	v_pk_fma_f32 v[44:45], v[50:51], v[138:139], v[44:45] op_sel_hi:[1,0,1]
	v_pk_add_f32 v[52:53], v[52:53], v[66:67]
	v_pk_fma_f32 v[4:5], v[66:67], v[160:161], v[4:5] op_sel_hi:[1,0,1]
	v_pk_fma_f32 v[8:9], v[66:67], v[160:161], v[8:9] op_sel:[0,1,0]
	v_pk_fma_f32 v[44:45], v[66:67], v[162:163], v[44:45] op_sel_hi:[1,0,1]
	s_waitcnt lgkmcnt(0)
	s_barrier
	s_add_i32 s5, s34, 9
	s_min_i32 s5, s5, 0x200
	s_mul_i32 s6, s5, 0x804
	s_add_i32 s6, s6, s35
	s_add_i32 s7, s6, 0x505014
	s_add_i32 s8, s6, 0x606018
	s_mul_i32 s9, s5, 0x180c
	s_add_i32 s9, s9, s33
	s_add_i32 s4, s34, 10
	s_min_i32 s4, s4, 0x200
	s_mul_i32 s4, s4, 0x804
	s_add_i32 s4, s4, s38
	buffer_load_dword v2, v28, s[20:23], s4 offen nt
	buffer_load_dwordx3 v[64:66], v27, s[24:27], s9 offen nt
	buffer_load_dword v50, v28, s[16:19], s7 offen nt
	buffer_load_dword v51, v28, s[16:19], s8 offen nt
	s_waitcnt vmcnt(8)
	s_add_i32 s4, s34, 8
	s_cmpk_lt_u32 s4, 0x201
	s_cselect_b64 s[12:13], s[40:41], 0
	v_cmp_eq_u32_e64 s[14:15], s37, v25
	s_and_b64 s[14:15], s[14:15], s[12:13]
	v_cndmask_b32_e64 v29, 0, 1, s[14:15]
	v_mov_b32_dpp v108, v144 wave_shr:1 row_mask:0xf bank_mask:0xf bound_ctrl:1
	v_mov_b32_dpp v109, v145 wave_shr:1 row_mask:0xf bank_mask:0xf bound_ctrl:1
	v_or_b32_dpp v90, v29, v29 wave_shr:1 row_mask:0xf bank_mask:0xf bound_ctrl:1
	v_mov_b32_dpp v110, v146 wave_shr:1 row_mask:0xf bank_mask:0xf bound_ctrl:1
	v_or_b32_dpp v90, v29, v90 wave_shl:1 row_mask:0xf bank_mask:0xf bound_ctrl:1
	v_mov_b32_dpp v152, v144 wave_shl:1 row_mask:0xf bank_mask:0xf bound_ctrl:1
	v_mov_b32_dpp v153, v145 wave_shl:1 row_mask:0xf bank_mask:0xf bound_ctrl:1
	v_or_b32_dpp v91, v90, v90 wave_shr:1 row_mask:0xf bank_mask:0xf bound_ctrl:1
	v_mov_b32_dpp v154, v146 wave_shl:1 row_mask:0xf bank_mask:0xf bound_ctrl:1
	v_or_b32_dpp v91, v90, v91 wave_shl:1 row_mask:0xf bank_mask:0xf bound_ctrl:1
	v_pk_add_f32 v[166:167], v[118:119], v[52:53]
	v_pk_add_f32 v[116:117], v[72:73], v[166:167]
	v_pk_add_f32 v[118:119], v[6:7], v[4:5]
	v_pk_add_f32 v[170:171], v[20:21], v[118:119]
	v_pk_add_f32 v[6:7], v[14:15], v[8:9]
	v_pk_add_f32 v[174:175], v[32:33], v[6:7]
	v_pk_add_f32 v[14:15], v[114:115], v[44:45]
	v_pk_add_f32 v[178:179], v[68:69], v[14:15]
	v_pk_fma_f32 v[170:171], v[76:77], v[116:117], v[170:171] op_sel_hi:[0,1,1] neg_lo:[1,0,0] neg_hi:[1,0,0]
	v_pk_fma_f32 v[174:175], v[76:77], v[116:117], v[174:175] op_sel:[1,0,0] neg_lo:[1,0,0] neg_hi:[1,0,0]
	v_pk_fma_f32 v[178:179], v[78:79], v[116:117], v[178:179] op_sel_hi:[0,1,1] neg_lo:[1,0,0] neg_hi:[1,0,0]
	v_pk_mul_f32 v[20:21], v[78:79], v[170:171] op_sel:[1,0]
	v_pk_mul_f32 v[32:33], v[100:101], v[170:171] op_sel_hi:[0,1]
	v_pk_mul_f32 v[68:69], v[100:101], v[170:171] op_sel:[1,0]
	v_pk_fma_f32 v[20:21], v[100:101], v[174:175], v[20:21] op_sel_hi:[0,1,1]
	v_pk_fma_f32 v[32:33], v[102:103], v[174:175], v[32:33] op_sel_hi:[0,1,1]
	v_pk_fma_f32 v[68:69], v[102:103], v[174:175], v[68:69] op_sel:[1,0,0]
	v_pk_fma_f32 v[20:21], v[100:101], v[178:179], v[20:21] op_sel:[1,0,0]
	v_pk_fma_f32 v[32:33], v[102:103], v[178:179], v[32:33] op_sel:[1,0,0]
	v_pk_fma_f32 v[68:69], v[104:105], v[178:179], v[68:69] op_sel_hi:[0,1,1]
	v_pk_mul_f32 v[114:115], v[76:77], v[20:21] op_sel_hi:[0,1]
	v_pk_fma_f32 v[114:115], v[76:77], v[32:33], v[114:115] op_sel:[1,0,0]
	v_pk_fma_f32 v[114:115], v[78:79], v[68:69], v[114:115] op_sel_hi:[0,1,1]
	v_pk_fma_f32 v[114:115], v[104:105], v[116:117], v[114:115] op_sel:[1,0,0] neg_lo:[0,0,1] neg_hi:[0,0,1]
	v_cmp_eq_u32_e64 s[10:11], 6, v107
	v_cmp_eq_u32_e64 s[14:15], 7, v107
	v_pk_add_f32 v[72:73], v[92:93], v[20:21]
	v_pk_add_f32 v[116:117], v[74:75], v[72:73]
	v_pk_add_f32 v[92:93], v[96:97], v[32:33]
	v_pk_add_f32 v[74:75], v[94:95], v[92:93]
	v_pk_add_f32 v[96:97], v[112:113], v[68:69]
	v_pk_add_f32 v[94:95], v[98:99], v[96:97]
	v_pk_add_f32 v[98:99], v[70:71], v[114:115]
	v_pk_add_f32 v[112:113], v[40:41], v[98:99]
	v_pk_fma_f32 v[40:41], v[124:125], v[116:117], v[112:113] op_sel_hi:[0,1,1]
	v_pk_fma_f32 v[164:165], v[140:141], v[116:117], v[112:113] op_sel_hi:[0,1,1]
	v_pk_fma_f32 v[40:41], v[124:125], v[74:75], v[40:41] op_sel:[1,0,0]
	v_pk_fma_f32 v[164:165], v[140:141], v[74:75], v[164:165] op_sel:[1,0,0]
	v_pk_fma_f32 v[40:41], v[126:127], v[94:95], v[40:41] op_sel_hi:[0,1,1]
	v_pk_fma_f32 v[164:165], v[142:143], v[94:95], v[164:165] op_sel_hi:[0,1,1]
	v_pk_fma_f32 v[112:113], v[132:133], v[116:117], v[112:113] op_sel_hi:[0,1,1]
	v_pk_fma_f32 v[112:113], v[132:133], v[74:75], v[112:113] op_sel:[1,0,0]
	v_pk_fma_f32 v[112:113], v[134:135], v[94:95], v[112:113] op_sel_hi:[0,1,1]
	v_cndmask_b32_e64 v70, 0, v18, s[10:11]
	v_cndmask_b32_e64 v71, 0, v18, s[14:15]
	v_add_f32_dpp v112, v40, v112 wave_shl:1 row_mask:0xf bank_mask:0xf bound_ctrl:1
	v_add_f32_dpp v113, v41, v113 wave_shl:1 row_mask:0xf bank_mask:0xf bound_ctrl:1
	s_add_i32 s4, s34, 4
	s_cmpk_lt_i32 s4, 0x201
	s_cselect_b64 s[12:13], s[0:1], 0
	v_add_f32_dpp v112, v164, v112 wave_shr:1 row_mask:0xf bank_mask:0xf bound_ctrl:1
	v_add_f32_dpp v113, v165, v113 wave_shr:1 row_mask:0xf bank_mask:0xf bound_ctrl:1
	v_pk_fma_f32 v[112:113], v[36:37], v[106:107], v[112:113] op_sel_hi:[1,0,1] neg_lo:[0,0,1] neg_hi:[0,0,1]
	v_pk_add_f32 v[112:113], v[112:113], v[70:71] neg_lo:[0,1] neg_hi:[0,1]
	v_pk_mul_f32 v[168:169], v[112:113], v[112:113]
	v_add_f32_e32 v168, v168, v169
	v_cndmask_b32_e64 v169, 0, v168, s[12:13]
	v_add_f32_e32 v1, v1, v169
	s_waitcnt vmcnt(8)
	v_pk_add_f32 v[36:37], v[144:145], v[108:109]
	v_pk_mul_f32 v[40:41], v[144:145], v[144:145] op_sel_hi:[0,1]
	v_pk_mul_f32 v[70:71], v[144:145], v[146:147] op_sel_hi:[1,0]
	v_mul_f32_e64 v74, v145, v145
	v_mul_f32_e64 v75, v146, v146
	v_add_f32_e64 v76, v146, v110
	v_pk_add_f32 v[36:37], v[36:37], v[152:153]
	v_or3_b32 v29, v91, v57, v58
	v_or3_b32 v29, v29, v59, v56
	s_add_i32 s4, s34, 5
	s_cmpk_lt_u32 s4, 0x1ff
	s_cselect_b64 s[12:13], s[42:43], 0
	v_cmp_ne_u32_e64 s[30:31], 0, v29
	s_and_b64 s[30:31], s[30:31], s[12:13]
	v_cndmask_b32_e64 v29, 0, 1.0, s[30:31]
	v_pk_fma_f32 v[40:41], v[108:109], v[108:109], v[40:41] op_sel_hi:[0,1,1]
	v_pk_fma_f32 v[70:71], v[108:109], v[110:111], v[70:71] op_sel_hi:[1,0,1]
	v_fma_f32 v74, v109, v109, v74
	v_fma_f32 v75, v110, v110, v75
	v_add_f32_dpp v77, v29, v29 wave_shr:1 row_mask:0xf bank_mask:0xf bound_ctrl:1
	v_add_f32_e64 v76, v76, v154
	v_pk_fma_f32 v[40:41], v[152:153], v[152:153], v[40:41] op_sel_hi:[0,1,1]
	v_pk_fma_f32 v[70:71], v[152:153], v[154:155], v[70:71] op_sel_hi:[1,0,1]
	v_fma_f32 v74, v153, v153, v74
	v_fma_f32 v75, v154, v154, v75
	v_add_f32_dpp v77, v29, v77 wave_shl:1 row_mask:0xf bank_mask:0xf bound_ctrl:1
	v_pk_add_f32 v[78:79], v[88:89], v[36:37]
	v_pk_add_f32 v[88:89], v[30:31], v[40:41]
	v_pk_add_f32 v[30:31], v[82:83], v[70:71]
	v_pk_add_f32 v[82:83], v[46:47], v[74:75]
	v_pk_add_f32 v[46:47], v[60:61], v[76:77]
	v_mul_f32_e64 v100, v78, v22
	v_mul_f32_e64 v101, v79, v22
	v_mul_f32_e64 v102, v46, v22
	v_fma_f32 v29, v88, v22, v26
	v_mul_f32_e64 v90, v89, v22
	v_mul_f32_e64 v60, v30, v22
	v_fma_f32 v61, v82, v22, v26
	v_mul_f32_e64 v94, v31, v22
	v_fma_f32 v95, v83, v22, v26
	v_fma_f32 v29, -v100, v100, v29
	v_fma_f32 v90, -v100, v101, v90
	v_fma_f32 v60, -v100, v102, v60
	v_fma_f32 v61, -v101, v101, v61
	v_fma_f32 v94, -v101, v102, v94
	v_fma_f32 v95, -v102, v102, v95
	v_mul_f32_e64 v112, v94, v94
	v_mul_f32_e64 v113, v90, v95
	v_mul_f32_e64 v116, v60, v61
	v_mul_f32_e64 v117, v60, v60
	v_mul_f32_e64 v132, v29, v94
	v_mul_f32_e64 v133, v90, v90
	v_fma_f32 v112, v61, v95, -v112
	v_fma_f32 v113, v60, v94, -v113
	v_fma_f32 v116, v90, v94, -v116
	v_fma_f32 v117, v29, v95, -v117
	v_fma_f32 v132, v90, v60, -v132
	v_fma_f32 v133, v29, v61, -v133
	v_mul_f32_e64 v134, v29, v112
	v_fma_f32 v134, v90, v113, v134
	v_fma_f32 v134, v60, v116, v134
	v_rcp_f32_e32 v134, v134
	v_cmp_ne_u32_e64 vcc, s37, v3
	v_mul_f32_e64 v134, v134, v22
	v_cndmask_b32_e64 v134, 0, v134, s[30:31]
	v_cndmask_b32_e64 v29, 0, v18, vcc
	v_cndmask_b32_e64 v125, 0, v22, s[30:31]
	v_mul_f32_e64 v103, v112, v134
	v_mul_f32_e64 v104, v113, v134
	v_mul_f32_e64 v105, v116, v134
	v_mul_f32_e64 v106, v117, v134
	v_mul_f32_e64 v107, v132, v134
	v_mul_f32_e64 v124, v133, v134
	v_add_f32_e64 v126, v47, v29
	v_mov_b32_e32 v127, v3
	ds_write_b128 v23, v[100:103] offset:3072
	ds_write_b128 v23, v[104:107] offset:4096
	ds_write_b128 v23, v[124:127] offset:5120
	v_mov_b32_dpp v60, v34 wave_shr:1 row_mask:0xf bank_mask:0xf bound_ctrl:1
	v_mov_b32_dpp v61, v35 wave_shr:1 row_mask:0xf bank_mask:0xf bound_ctrl:1
	v_mov_b32_dpp v88, v34 wave_shl:1 row_mask:0xf bank_mask:0xf bound_ctrl:1
	v_mov_b32_dpp v89, v35 wave_shl:1 row_mask:0xf bank_mask:0xf bound_ctrl:1
	v_pk_mul_f32 v[30:31], v[34:35], v[144:145] op_sel_hi:[1,0]
	v_pk_mul_f32 v[46:47], v[34:35], v[144:145] op_sel:[0,1]
	v_pk_mul_f32 v[78:79], v[34:35], v[146:147] op_sel_hi:[1,0]
	v_pk_add_f32 v[82:83], v[34:35], v[60:61]
	v_pk_fma_f32 v[30:31], v[60:61], v[108:109], v[30:31] op_sel_hi:[1,0,1]
	v_pk_fma_f32 v[46:47], v[60:61], v[108:109], v[46:47] op_sel:[0,1,0]
	v_pk_fma_f32 v[78:79], v[60:61], v[110:111], v[78:79] op_sel_hi:[1,0,1]
	v_pk_add_f32 v[82:83], v[82:83], v[88:89]
	v_pk_fma_f32 v[30:31], v[88:89], v[152:153], v[30:31] op_sel_hi:[1,0,1]
	v_pk_fma_f32 v[46:47], v[88:89], v[152:153], v[46:47] op_sel:[0,1,0]
	v_pk_fma_f32 v[78:79], v[88:89], v[154:155], v[78:79] op_sel_hi:[1,0,1]
	s_waitcnt lgkmcnt(0)
	s_barrier
	s_add_i32 s5, s34, 10
	s_min_i32 s5, s5, 0x200
	s_mul_i32 s6, s5, 0x804
	s_add_i32 s6, s6, s35
	s_add_i32 s7, s6, 0x505014
	s_add_i32 s8, s6, 0x606018
	s_mul_i32 s9, s5, 0x180c
	s_add_i32 s9, s9, s33
	s_add_i32 s4, s34, 11
	s_min_i32 s4, s4, 0x200
	s_mul_i32 s4, s4, 0x804
	s_add_i32 s4, s4, s38
	buffer_load_dword v3, v28, s[20:23], s4 offen nt
	buffer_load_dwordx3 v[132:134], v27, s[24:27], s9 offen nt
	buffer_load_dword v60, v28, s[16:19], s7 offen nt
	buffer_load_dword v61, v28, s[16:19], s8 offen nt
	s_waitcnt vmcnt(8)
	s_add_i32 s4, s34, 9
	s_cmpk_lt_u32 s4, 0x201
	s_cselect_b64 s[12:13], s[40:41], 0
	v_cmp_eq_u32_e64 s[14:15], s37, v24
	s_and_b64 s[14:15], s[14:15], s[12:13]
	v_cndmask_b32_e64 v29, 0, 1, s[14:15]
	v_mov_b32_dpp v140, v120 wave_shr:1 row_mask:0xf bank_mask:0xf bound_ctrl:1
	v_mov_b32_dpp v141, v121 wave_shr:1 row_mask:0xf bank_mask:0xf bound_ctrl:1
	v_or_b32_dpp v56, v29, v29 wave_shr:1 row_mask:0xf bank_mask:0xf bound_ctrl:1
	v_mov_b32_dpp v142, v122 wave_shr:1 row_mask:0xf bank_mask:0xf bound_ctrl:1
	v_or_b32_dpp v56, v29, v56 wave_shl:1 row_mask:0xf bank_mask:0xf bound_ctrl:1
	v_mov_b32_dpp v168, v120 wave_shl:1 row_mask:0xf bank_mask:0xf bound_ctrl:1
	v_mov_b32_dpp v169, v121 wave_shl:1 row_mask:0xf bank_mask:0xf bound_ctrl:1
	v_or_b32_dpp v90, v56, v56 wave_shr:1 row_mask:0xf bank_mask:0xf bound_ctrl:1
	v_mov_b32_dpp v170, v122 wave_shl:1 row_mask:0xf bank_mask:0xf bound_ctrl:1
	v_or_b32_dpp v90, v56, v90 wave_shl:1 row_mask:0xf bank_mask:0xf bound_ctrl:1
	v_pk_add_f32 v[88:89], v[166:167], v[82:83]
	v_pk_add_f32 v[94:95], v[118:119], v[30:31]
	v_pk_add_f32 v[118:119], v[6:7], v[46:47]
	v_pk_add_f32 v[6:7], v[14:15], v[78:79]
	v_pk_fma_f32 v[94:95], v[100:101], v[88:89], v[94:95] op_sel_hi:[0,1,1] neg_lo:[1,0,0] neg_hi:[1,0,0]
	v_pk_fma_f32 v[118:119], v[100:101], v[88:89], v[118:119] op_sel:[1,0,0] neg_lo:[1,0,0] neg_hi:[1,0,0]
	v_pk_fma_f32 v[6:7], v[102:103], v[88:89], v[6:7] op_sel_hi:[0,1,1] neg_lo:[1,0,0] neg_hi:[1,0,0]
	v_pk_mul_f32 v[112:113], v[102:103], v[94:95] op_sel:[1,0]
	v_pk_mul_f32 v[116:117], v[104:105], v[94:95] op_sel_hi:[0,1]
	v_pk_mul_f32 v[164:165], v[104:105], v[94:95] op_sel:[1,0]
	v_pk_fma_f32 v[112:113], v[104:105], v[118:119], v[112:113] op_sel_hi:[0,1,1]
	v_pk_fma_f32 v[116:117], v[106:107], v[118:119], v[116:117] op_sel_hi:[0,1,1]
	v_pk_fma_f32 v[164:165], v[106:107], v[118:119], v[164:165] op_sel:[1,0,0]
	v_pk_fma_f32 v[112:113], v[104:105], v[6:7], v[112:113] op_sel:[1,0,0]
	v_pk_fma_f32 v[116:117], v[106:107], v[6:7], v[116:117] op_sel:[1,0,0]
	v_pk_fma_f32 v[164:165], v[124:125], v[6:7], v[164:165] op_sel_hi:[0,1,1]
	v_pk_mul_f32 v[14:15], v[100:101], v[112:113] op_sel_hi:[0,1]
	v_pk_fma_f32 v[14:15], v[100:101], v[116:117], v[14:15] op_sel:[1,0,0]
	v_pk_fma_f32 v[14:15], v[102:103], v[164:165], v[14:15] op_sel_hi:[0,1,1]
	v_pk_fma_f32 v[14:15], v[124:125], v[88:89], v[14:15] op_sel:[1,0,0] neg_lo:[0,0,1] neg_hi:[0,0,1]
	v_cmp_eq_u32_e64 s[10:11], 6, v127
	v_cmp_eq_u32_e64 s[14:15], 7, v127
	v_pk_add_f32 v[6:7], v[72:73], v[112:113]
	v_pk_add_f32 v[72:73], v[92:93], v[116:117]
	v_pk_add_f32 v[88:89], v[96:97], v[164:165]
	v_pk_add_f32 v[94:95], v[98:99], v[14:15]
	v_pk_fma_f32 v[98:99], v[148:149], v[6:7], v[94:95] op_sel_hi:[0,1,1]
	v_pk_fma_f32 v[118:119], v[156:157], v[6:7], v[94:95] op_sel_hi:[0,1,1]
	v_pk_fma_f32 v[98:99], v[148:149], v[72:73], v[98:99] op_sel:[1,0,0]
	v_pk_fma_f32 v[118:119], v[156:157], v[72:73], v[118:119] op_sel:[1,0,0]
	v_pk_fma_f32 v[98:99], v[150:151], v[88:89], v[98:99] op_sel_hi:[0,1,1]
	v_pk_fma_f32 v[118:119], v[158:159], v[88:89], v[118:119] op_sel_hi:[0,1,1]
	v_pk_fma_f32 v[94:95], v[128:129], v[6:7], v[94:95] op_sel_hi:[0,1,1]
	v_pk_fma_f32 v[94:95], v[128:129], v[72:73], v[94:95] op_sel:[1,0,0]
	v_pk_fma_f32 v[94:95], v[130:131], v[88:89], v[94:95] op_sel_hi:[0,1,1]
	v_cndmask_b32_e64 v92, 0, v18, s[10:11]
	v_cndmask_b32_e64 v93, 0, v18, s[14:15]
	v_add_f32_dpp v94, v98, v94 wave_shl:1 row_mask:0xf bank_mask:0xf bound_ctrl:1
	v_add_f32_dpp v95, v99, v95 wave_shl:1 row_mask:0xf bank_mask:0xf bound_ctrl:1
	s_add_i32 s4, s34, 5
	s_cmpk_lt_i32 s4, 0x201
	s_cselect_b64 s[12:13], s[0:1], 0
	v_add_f32_dpp v94, v118, v94 wave_shr:1 row_mask:0xf bank_mask:0xf bound_ctrl:1
	v_add_f32_dpp v95, v119, v95 wave_shr:1 row_mask:0xf bank_mask:0xf bound_ctrl:1
	v_pk_fma_f32 v[94:95], v[10:11], v[126:127], v[94:95] op_sel_hi:[1,0,1] neg_lo:[0,0,1] neg_hi:[0,0,1]
	v_pk_add_f32 v[94:95], v[94:95], v[92:93] neg_lo:[0,1] neg_hi:[0,1]
	v_pk_mul_f32 v[96:97], v[94:95], v[94:95]
	v_add_f32_e32 v96, v96, v97
	v_cndmask_b32_e64 v97, 0, v96, s[12:13]
	v_add_f32_e32 v1, v1, v97
	s_waitcnt vmcnt(8)
	v_pk_add_f32 v[6:7], v[120:121], v[140:141]
	v_pk_mul_f32 v[10:11], v[120:121], v[120:121] op_sel_hi:[0,1]
	v_pk_mul_f32 v[72:73], v[120:121], v[122:123] op_sel_hi:[1,0]
	v_mul_f32_e64 v88, v121, v121
	v_mul_f32_e64 v89, v122, v122
	v_add_f32_e64 v92, v122, v142
	v_pk_add_f32 v[6:7], v[6:7], v[168:169]
	v_or3_b32 v29, v90, v91, v57
	v_or3_b32 v29, v29, v58, v59
	s_add_i32 s4, s34, 6
	s_cmpk_lt_u32 s4, 0x1ff
	s_cselect_b64 s[12:13], s[42:43], 0
	v_cmp_ne_u32_e64 s[30:31], 0, v29
	s_and_b64 s[30:31], s[30:31], s[12:13]
	v_cndmask_b32_e64 v29, 0, 1.0, s[30:31]
	v_pk_fma_f32 v[10:11], v[140:141], v[140:141], v[10:11] op_sel_hi:[0,1,1]
	v_pk_fma_f32 v[72:73], v[140:141], v[142:143], v[72:73] op_sel_hi:[1,0,1]
	v_fma_f32 v88, v141, v141, v88
	v_fma_f32 v89, v142, v142, v89
	v_add_f32_dpp v93, v29, v29 wave_shr:1 row_mask:0xf bank_mask:0xf bound_ctrl:1
	v_add_f32_e64 v92, v92, v170
	v_pk_fma_f32 v[10:11], v[168:169], v[168:169], v[10:11] op_sel_hi:[0,1,1]
	v_pk_fma_f32 v[72:73], v[168:169], v[170:171], v[72:73] op_sel_hi:[1,0,1]
	v_fma_f32 v88, v169, v169, v88
	v_fma_f32 v89, v170, v170, v89
	v_add_f32_dpp v93, v29, v93 wave_shl:1 row_mask:0xf bank_mask:0xf bound_ctrl:1
	v_pk_add_f32 v[96:97], v[36:37], v[6:7]
	v_pk_add_f32 v[94:95], v[38:39], v[96:97]
	v_pk_add_f32 v[36:37], v[40:41], v[10:11]
	v_pk_add_f32 v[38:39], v[42:43], v[36:37]
	v_pk_add_f32 v[42:43], v[70:71], v[72:73]
	v_pk_add_f32 v[40:41], v[48:49], v[42:43]
	v_pk_add_f32 v[48:49], v[74:75], v[88:89]
	v_pk_add_f32 v[70:71], v[54:55], v[48:49]
	v_pk_add_f32 v[100:101], v[76:77], v[92:93]
	v_pk_add_f32 v[54:55], v[62:63], v[100:101]
	v_mul_f32_e64 v104, v94, v22
	v_mul_f32_e64 v105, v95, v22
	v_mul_f32_e64 v106, v54, v22
	v_fma_f32 v29, v38, v22, v26
	v_mul_f32_e64 v56, v39, v22
	v_mul_f32_e64 v62, v40, v22
	v_fma_f32 v63, v70, v22, v26
	v_mul_f32_e64 v74, v41, v22
	v_fma_f32 v75, v71, v22, v26
	v_fma_f32 v29, -v104, v104, v29
	v_fma_f32 v56, -v104, v105, v56
	v_fma_f32 v62, -v104, v106, v62
	v_fma_f32 v63, -v105, v105, v63
	v_fma_f32 v74, -v105, v106, v74
	v_fma_f32 v75, -v106, v106, v75
	v_mul_f32_e64 v76, v74, v74
	v_mul_f32_e64 v77, v56, v75
	v_mul_f32_e64 v98, v62, v63
	v_mul_f32_e64 v99, v62, v62
	v_mul_f32_e64 v102, v29, v74
	v_mul_f32_e64 v103, v56, v56
	v_fma_f32 v76, v63, v75, -v76
	v_fma_f32 v77, v62, v74, -v77
	v_fma_f32 v98, v56, v74, -v98
	v_fma_f32 v99, v29, v75, -v99
	v_fma_f32 v102, v56, v62, -v102
	v_fma_f32 v103, v29, v63, -v103
	v_mul_f32_e64 v118, v29, v76
	v_fma_f32 v118, v56, v77, v118
	v_fma_f32 v118, v62, v98, v118
	v_rcp_f32_e32 v118, v118
	v_cmp_ne_u32_e64 vcc, s37, v16
	v_mul_f32_e64 v118, v118, v22
	v_cndmask_b32_e64 v118, 0, v118, s[30:31]
	v_cndmask_b32_e64 v29, 0, v18, vcc
	v_cndmask_b32_e64 v129, 0, v22, s[30:31]
	v_mul_f32_e64 v107, v76, v118
	v_mul_f32_e64 v124, v77, v118
	v_mul_f32_e64 v125, v98, v118
	v_mul_f32_e64 v126, v99, v118
	v_mul_f32_e64 v127, v102, v118
	v_mul_f32_e64 v128, v103, v118
	v_add_f32_e64 v130, v55, v29
	v_mov_b32_e32 v131, v16
	ds_write_b128 v23, v[104:107]
	ds_write_b128 v23, v[124:127] offset:1024
	ds_write_b128 v23, v[128:131] offset:2048
	v_mov_b32_dpp v38, v12 wave_shr:1 row_mask:0xf bank_mask:0xf bound_ctrl:1
	v_mov_b32_dpp v39, v13 wave_shr:1 row_mask:0xf bank_mask:0xf bound_ctrl:1
	v_mov_b32_dpp v54, v12 wave_shl:1 row_mask:0xf bank_mask:0xf bound_ctrl:1
	v_mov_b32_dpp v55, v13 wave_shl:1 row_mask:0xf bank_mask:0xf bound_ctrl:1
	v_pk_mul_f32 v[40:41], v[12:13], v[120:121] op_sel_hi:[1,0]
	v_pk_mul_f32 v[76:77], v[12:13], v[120:121] op_sel:[0,1]
	v_pk_mul_f32 v[148:149], v[12:13], v[122:123] op_sel_hi:[1,0]
	v_pk_add_f32 v[156:157], v[12:13], v[38:39]
	v_pk_fma_f32 v[40:41], v[38:39], v[140:141], v[40:41] op_sel_hi:[1,0,1]
	v_pk_fma_f32 v[76:77], v[38:39], v[140:141], v[76:77] op_sel:[0,1,0]
	v_pk_fma_f32 v[148:149], v[38:39], v[142:143], v[148:149] op_sel_hi:[1,0,1]
	v_pk_add_f32 v[156:157], v[156:157], v[54:55]
	v_pk_fma_f32 v[40:41], v[54:55], v[168:169], v[40:41] op_sel_hi:[1,0,1]
	v_pk_fma_f32 v[76:77], v[54:55], v[168:169], v[76:77] op_sel:[0,1,0]
	v_pk_fma_f32 v[148:149], v[54:55], v[170:171], v[148:149] op_sel_hi:[1,0,1]
	s_waitcnt lgkmcnt(0)
	s_barrier
	s_add_i32 s5, s34, 11
	s_min_i32 s5, s5, 0x200
	s_mul_i32 s6, s5, 0x804
	s_add_i32 s6, s6, s35
	s_add_i32 s7, s6, 0x505014
	s_add_i32 s8, s6, 0x606018
	s_mul_i32 s9, s5, 0x180c
	s_add_i32 s9, s9, s33
	s_add_i32 s4, s34, 12
	s_min_i32 s4, s4, 0x200
	s_mul_i32 s4, s4, 0x804
	s_add_i32 s4, s4, s38
	buffer_load_dword v16, v28, s[20:23], s4 offen nt
	buffer_load_dwordx3 v[172:174], v27, s[24:27], s9 offen nt
	buffer_load_dword v38, v28, s[16:19], s7 offen nt
	buffer_load_dword v39, v28, s[16:19], s8 offen nt
	s_waitcnt vmcnt(8)
	s_add_i32 s4, s34, 10
	s_cmpk_lt_u32 s4, 0x201
	s_cselect_b64 s[12:13], s[40:41], 0
	v_cmp_eq_u32_e64 s[14:15], s37, v2
	s_and_b64 s[14:15], s[14:15], s[12:13]
	v_cndmask_b32_e64 v29, 0, 1, s[14:15]
	v_mov_b32_dpp v176, v64 wave_shr:1 row_mask:0xf bank_mask:0xf bound_ctrl:1
	v_mov_b32_dpp v177, v65 wave_shr:1 row_mask:0xf bank_mask:0xf bound_ctrl:1
	v_or_b32_dpp v56, v29, v29 wave_shr:1 row_mask:0xf bank_mask:0xf bound_ctrl:1
	v_mov_b32_dpp v178, v66 wave_shr:1 row_mask:0xf bank_mask:0xf bound_ctrl:1
	v_or_b32_dpp v56, v29, v56 wave_shl:1 row_mask:0xf bank_mask:0xf bound_ctrl:1
	v_mov_b32_dpp v180, v64 wave_shl:1 row_mask:0xf bank_mask:0xf bound_ctrl:1
	v_mov_b32_dpp v181, v65 wave_shl:1 row_mask:0xf bank_mask:0xf bound_ctrl:1
	v_or_b32_dpp v59, v56, v56 wave_shr:1 row_mask:0xf bank_mask:0xf bound_ctrl:1
	v_mov_b32_dpp v182, v66 wave_shl:1 row_mask:0xf bank_mask:0xf bound_ctrl:1
	v_or_b32_dpp v59, v56, v59 wave_shl:1 row_mask:0xf bank_mask:0xf bound_ctrl:1
	v_pk_add_f32 v[54:55], v[82:83], v[156:157]
	v_pk_add_f32 v[62:63], v[52:53], v[54:55]
	v_pk_add_f32 v[70:71], v[30:31], v[40:41]
	v_pk_add_f32 v[52:53], v[4:5], v[70:71]
	v_pk_add_f32 v[30:31], v[46:47], v[76:77]
	v_pk_add_f32 v[4:5], v[8:9], v[30:31]
	v_pk_add_f32 v[46:47], v[78:79], v[148:149]
	v_pk_add_f32 v[8:9], v[44:45], v[46:47]
	v_pk_fma_f32 v[52:53], v[104:105], v[62:63], v[52:53] op_sel_hi:[0,1,1] neg_lo:[1,0,0] neg_hi:[1,0,0]
	v_pk_fma_f32 v[4:5], v[104:105], v[62:63], v[4:5] op_sel:[1,0,0] neg_lo:[1,0,0] neg_hi:[1,0,0]
	v_pk_fma_f32 v[8:9], v[106:107], v[62:63], v[8:9] op_sel_hi:[0,1,1] neg_lo:[1,0,0] neg_hi:[1,0,0]
	v_pk_mul_f32 v[74:75], v[106:107], v[52:53] op_sel:[1,0]
	v_pk_mul_f32 v[78:79], v[124:125], v[52:53] op_sel_hi:[0,1]
	v_pk_mul_f32 v[82:83], v[124:125], v[52:53] op_sel:[1,0]
	v_pk_fma_f32 v[74:75], v[124:125], v[4:5], v[74:75] op_sel_hi:[0,1,1]
	v_pk_fma_f32 v[78:79], v[126:127], v[4:5], v[78:79] op_sel_hi:[0,1,1]
	v_pk_fma_f32 v[82:83], v[126:127], v[4:5], v[82:83] op_sel:[1,0,0]
	v_pk_fma_f32 v[74:75], v[124:125], v[8:9], v[74:75] op_sel:[1,0,0]
	v_pk_fma_f32 v[78:79], v[126:127], v[8:9], v[78:79] op_sel:[1,0,0]
	v_pk_fma_f32 v[82:83], v[128:129], v[8:9], v[82:83] op_sel_hi:[0,1,1]
	v_pk_mul_f32 v[44:45], v[104:105], v[74:75] op_sel_hi:[0,1]
	v_pk_fma_f32 v[44:45], v[104:105], v[78:79], v[44:45] op_sel:[1,0,0]
	v_pk_fma_f32 v[44:45], v[106:107], v[82:83], v[44:45] op_sel_hi:[0,1,1]
	v_pk_fma_f32 v[44:45], v[128:129], v[62:63], v[44:45] op_sel:[1,0,0] neg_lo:[0,0,1] neg_hi:[0,0,1]
	v_cmp_eq_u32_e64 s[10:11], 6, v131
	v_cmp_eq_u32_e64 s[14:15], 7, v131
	v_pk_add_f32 v[62:63], v[112:113], v[74:75]
	v_pk_add_f32 v[4:5], v[20:21], v[62:63]
	v_pk_add_f32 v[94:95], v[116:117], v[78:79]
	v_pk_add_f32 v[8:9], v[32:33], v[94:95]
	v_pk_add_f32 v[98:99], v[164:165], v[82:83]
	v_pk_add_f32 v[20:21], v[68:69], v[98:99]
	v_pk_add_f32 v[32:33], v[14:15], v[44:45]
	v_pk_add_f32 v[102:103], v[114:115], v[32:33]
	v_pk_fma_f32 v[14:15], v[136:137], v[4:5], v[102:103] op_sel_hi:[0,1,1]
	v_pk_fma_f32 v[114:115], v[160:161], v[4:5], v[102:103] op_sel_hi:[0,1,1]
	v_pk_fma_f32 v[14:15], v[136:137], v[8:9], v[14:15] op_sel:[1,0,0]
	v_pk_fma_f32 v[114:115], v[160:161], v[8:9], v[114:115] op_sel:[1,0,0]
	v_pk_fma_f32 v[14:15], v[138:139], v[20:21], v[14:15] op_sel_hi:[0,1,1]
	v_pk_fma_f32 v[114:115], v[162:163], v[20:21], v[114:115] op_sel_hi:[0,1,1]
	v_pk_fma_f32 v[102:103], v[84:85], v[4:5], v[102:103] op_sel_hi:[0,1,1]
	v_pk_fma_f32 v[102:103], v[84:85], v[8:9], v[102:103] op_sel:[1,0,0]
	v_pk_fma_f32 v[102:103], v[86:87], v[20:21], v[102:103] op_sel_hi:[0,1,1]
	v_cndmask_b32_e64 v52, 0, v18, s[10:11]
	v_cndmask_b32_e64 v53, 0, v18, s[14:15]
	v_add_f32_dpp v102, v14, v102 wave_shl:1 row_mask:0xf bank_mask:0xf bound_ctrl:1
	v_add_f32_dpp v103, v15, v103 wave_shl:1 row_mask:0xf bank_mask:0xf bound_ctrl:1
	s_add_i32 s4, s34, 6
	s_cmpk_lt_i32 s4, 0x201
	s_cselect_b64 s[12:13], s[0:1], 0
	v_add_f32_dpp v102, v114, v102 wave_shr:1 row_mask:0xf bank_mask:0xf bound_ctrl:1
	v_add_f32_dpp v103, v115, v103 wave_shr:1 row_mask:0xf bank_mask:0xf bound_ctrl:1
	v_pk_fma_f32 v[102:103], v[80:81], v[130:131], v[102:103] op_sel_hi:[1,0,1] neg_lo:[0,0,1] neg_hi:[0,0,1]
	v_pk_add_f32 v[102:103], v[102:103], v[52:53] neg_lo:[0,1] neg_hi:[0,1]
	v_pk_mul_f32 v[68:69], v[102:103], v[102:103]
	v_add_f32_e32 v68, v68, v69
	v_cndmask_b32_e64 v69, 0, v68, s[12:13]
	v_add_f32_e32 v1, v1, v69
	s_waitcnt vmcnt(8)
	v_pk_add_f32 v[4:5], v[64:65], v[176:177]
	v_pk_mul_f32 v[8:9], v[64:65], v[64:65] op_sel_hi:[0,1]
	v_pk_mul_f32 v[14:15], v[64:65], v[66:67] op_sel_hi:[1,0]
	v_mul_f32_e64 v20, v65, v65
	v_mul_f32_e64 v21, v66, v66
	v_add_f32_e64 v52, v66, v178
	v_pk_add_f32 v[4:5], v[4:5], v[180:181]
	v_or3_b32 v29, v59, v90, v91
	v_or3_b32 v29, v29, v57, v58
	s_add_i32 s4, s34, 7
	s_cmpk_lt_u32 s4, 0x1ff
	s_cselect_b64 s[12:13], s[42:43], 0
	v_cmp_ne_u32_e64 s[30:31], 0, v29
	s_and_b64 s[30:31], s[30:31], s[12:13]
	v_cndmask_b32_e64 v29, 0, 1.0, s[30:31]
	v_pk_fma_f32 v[8:9], v[176:177], v[176:177], v[8:9] op_sel_hi:[0,1,1]
	v_pk_fma_f32 v[14:15], v[176:177], v[178:179], v[14:15] op_sel_hi:[1,0,1]
	v_fma_f32 v20, v177, v177, v20
	v_fma_f32 v21, v178, v178, v21
	v_add_f32_dpp v53, v29, v29 wave_shr:1 row_mask:0xf bank_mask:0xf bound_ctrl:1
	v_add_f32_e64 v52, v52, v182
	v_pk_fma_f32 v[8:9], v[180:181], v[180:181], v[8:9] op_sel_hi:[0,1,1]
	v_pk_fma_f32 v[14:15], v[180:181], v[182:183], v[14:15] op_sel_hi:[1,0,1]
	v_fma_f32 v20, v181, v181, v20
	v_fma_f32 v21, v182, v182, v21
	v_add_f32_dpp v53, v29, v53 wave_shl:1 row_mask:0xf bank_mask:0xf bound_ctrl:1
	v_pk_add_f32 v[68:69], v[96:97], v[4:5]
	v_pk_add_f32 v[80:81], v[36:37], v[8:9]
	v_pk_add_f32 v[36:37], v[42:43], v[14:15]
	v_pk_add_f32 v[42:43], v[48:49], v[20:21]
	v_pk_add_f32 v[48:49], v[100:101], v[52:53]
	v_mul_f32_e64 v84, v68, v22
	v_mul_f32_e64 v85, v69, v22
	v_mul_f32_e64 v86, v48, v22
	v_fma_f32 v29, v80, v22, v26
	v_mul_f32_e64 v56, v81, v22
	v_mul_f32_e64 v96, v36, v22
	v_fma_f32 v97, v42, v22, v26
	v_mul_f32_e64 v112, v37, v22
	v_fma_f32 v113, v43, v22, v26
	v_fma_f32 v29, -v84, v84, v29
	v_fma_f32 v56, -v84, v85, v56
	v_fma_f32 v96, -v84, v86, v96
	v_fma_f32 v97, -v85, v85, v97
	v_fma_f32 v112, -v85, v86, v112
	v_fma_f32 v113, -v86, v86, v113
	v_mul_f32_e64 v114, v112, v112
	v_mul_f32_e64 v115, v56, v113
	v_mul_f32_e64 v116, v96, v97
	v_mul_f32_e64 v117, v96, v96
	v_mul_f32_e64 v118, v29, v112
	v_mul_f32_e64 v119, v56, v56
	v_fma_f32 v114, v97, v113, -v114
	v_fma_f32 v115, v96, v112, -v115
	v_fma_f32 v116, v56, v112, -v116
	v_fma_f32 v117, v29, v113, -v117
	v_fma_f32 v118, v56, v96, -v118
	v_fma_f32 v119, v29, v97, -v119
	v_mul_f32_e64 v124, v29, v114
	v_fma_f32 v124, v56, v115, v124
	v_fma_f32 v124, v96, v116, v124
	v_rcp_f32_e32 v124, v124
	v_cmp_ne_u32_e64 vcc, s37, v17
	v_mul_f32_e64 v124, v124, v22
	v_cndmask_b32_e64 v124, 0, v124, s[30:31]
	v_cndmask_b32_e64 v29, 0, v18, vcc
	v_cndmask_b32_e64 v105, 0, v22, s[30:31]
	v_mul_f32_e64 v87, v114, v124
	v_mul_f32_e64 v100, v115, v124
	v_mul_f32_e64 v101, v116, v124
	v_mul_f32_e64 v102, v117, v124
	v_mul_f32_e64 v103, v118, v124
	v_mul_f32_e64 v104, v119, v124
	v_add_f32_e64 v106, v49, v29
	v_mov_b32_e32 v107, v17
	ds_write_b128 v23, v[84:87] offset:3072
	ds_write_b128 v23, v[100:103] offset:4096
	ds_write_b128 v23, v[104:107] offset:5120
	v_mov_b32_dpp v36, v50 wave_shr:1 row_mask:0xf bank_mask:0xf bound_ctrl:1
	v_mov_b32_dpp v37, v51 wave_shr:1 row_mask:0xf bank_mask:0xf bound_ctrl:1
	v_mov_b32_dpp v48, v50 wave_shl:1 row_mask:0xf bank_mask:0xf bound_ctrl:1
	v_mov_b32_dpp v49, v51 wave_shl:1 row_mask:0xf bank_mask:0xf bound_ctrl:1
	v_pk_mul_f32 v[42:43], v[50:51], v[64:65] op_sel_hi:[1,0]
	v_pk_mul_f32 v[114:115], v[50:51], v[64:65] op_sel:[0,1]
	v_pk_mul_f32 v[118:119], v[50:51], v[66:67] op_sel_hi:[1,0]
	v_pk_add_f32 v[126:127], v[50:51], v[36:37]
	v_pk_fma_f32 v[42:43], v[36:37], v[176:177], v[42:43] op_sel_hi:[1,0,1]
	v_pk_fma_f32 v[114:115], v[36:37], v[176:177], v[114:115] op_sel:[0,1,0]
	v_pk_fma_f32 v[118:119], v[36:37], v[178:179], v[118:119] op_sel_hi:[1,0,1]
	v_pk_add_f32 v[126:127], v[126:127], v[48:49]
	v_pk_fma_f32 v[42:43], v[48:49], v[180:181], v[42:43] op_sel_hi:[1,0,1]
	v_pk_fma_f32 v[114:115], v[48:49], v[180:181], v[114:115] op_sel:[0,1,0]
	v_pk_fma_f32 v[118:119], v[48:49], v[182:183], v[118:119] op_sel_hi:[1,0,1]
	s_waitcnt lgkmcnt(0)
	s_barrier
	s_waitcnt vmcnt(4)
	s_add_i32 s4, s34, 11
	s_cmpk_lt_u32 s4, 0x201
	s_cselect_b64 s[12:13], s[40:41], 0
	v_cmp_eq_u32_e64 s[14:15], s37, v3
	s_and_b64 s[14:15], s[14:15], s[12:13]
	v_cndmask_b32_e64 v17, 0, 1, s[14:15]
	v_mov_b32_dpp v128, v132 wave_shr:1 row_mask:0xf bank_mask:0xf bound_ctrl:1
	v_mov_b32_dpp v129, v133 wave_shr:1 row_mask:0xf bank_mask:0xf bound_ctrl:1
	v_or_b32_dpp v29, v17, v17 wave_shr:1 row_mask:0xf bank_mask:0xf bound_ctrl:1
	v_mov_b32_dpp v130, v134 wave_shr:1 row_mask:0xf bank_mask:0xf bound_ctrl:1
	v_or_b32_dpp v29, v17, v29 wave_shl:1 row_mask:0xf bank_mask:0xf bound_ctrl:1
	v_mov_b32_dpp v136, v132 wave_shl:1 row_mask:0xf bank_mask:0xf bound_ctrl:1
	v_mov_b32_dpp v137, v133 wave_shl:1 row_mask:0xf bank_mask:0xf bound_ctrl:1
	v_or_b32_dpp v56, v29, v29 wave_shr:1 row_mask:0xf bank_mask:0xf bound_ctrl:1
	v_mov_b32_dpp v138, v134 wave_shl:1 row_mask:0xf bank_mask:0xf bound_ctrl:1
	v_or_b32_dpp v56, v29, v56 wave_shl:1 row_mask:0xf bank_mask:0xf bound_ctrl:1
	v_pk_add_f32 v[36:37], v[54:55], v[126:127]
	v_pk_add_f32 v[54:55], v[70:71], v[42:43]
	v_pk_add_f32 v[70:71], v[30:31], v[114:115]
	v_pk_add_f32 v[30:31], v[46:47], v[118:119]
	v_pk_fma_f32 v[54:55], v[84:85], v[36:37], v[54:55] op_sel_hi:[0,1,1] neg_lo:[1,0,0] neg_hi:[1,0,0]
	v_pk_fma_f32 v[70:71], v[84:85], v[36:37], v[70:71] op_sel:[1,0,0] neg_lo:[1,0,0] neg_hi:[1,0,0]
	v_pk_fma_f32 v[30:31], v[86:87], v[36:37], v[30:31] op_sel_hi:[0,1,1] neg_lo:[1,0,0] neg_hi:[1,0,0]
	v_pk_mul_f32 v[48:49], v[86:87], v[54:55] op_sel:[1,0]
	v_pk_mul_f32 v[68:69], v[100:101], v[54:55] op_sel_hi:[0,1]
	v_pk_mul_f32 v[80:81], v[100:101], v[54:55] op_sel:[1,0]
	v_pk_fma_f32 v[48:49], v[100:101], v[70:71], v[48:49] op_sel_hi:[0,1,1]
	v_pk_fma_f32 v[68:69], v[102:103], v[70:71], v[68:69] op_sel_hi:[0,1,1]
	v_pk_fma_f32 v[80:81], v[102:103], v[70:71], v[80:81] op_sel:[1,0,0]
	v_pk_fma_f32 v[48:49], v[100:101], v[30:31], v[48:49] op_sel:[1,0,0]
	v_pk_fma_f32 v[68:69], v[102:103], v[30:31], v[68:69] op_sel:[1,0,0]
	v_pk_fma_f32 v[80:81], v[104:105], v[30:31], v[80:81] op_sel_hi:[0,1,1]
	v_pk_mul_f32 v[46:47], v[84:85], v[48:49] op_sel_hi:[0,1]
	v_pk_fma_f32 v[46:47], v[84:85], v[68:69], v[46:47] op_sel:[1,0,0]
	v_pk_fma_f32 v[46:47], v[86:87], v[80:81], v[46:47] op_sel_hi:[0,1,1]
	v_pk_fma_f32 v[46:47], v[104:105], v[36:37], v[46:47] op_sel:[1,0,0] neg_lo:[0,0,1] neg_hi:[0,0,1]
	v_cmp_eq_u32_e64 s[10:11], 6, v107
	v_cmp_eq_u32_e64 s[14:15], 7, v107
	v_pk_add_f32 v[30:31], v[62:63], v[48:49]
	v_pk_add_f32 v[36:37], v[94:95], v[68:69]
	v_pk_add_f32 v[54:55], v[98:99], v[80:81]
	v_pk_add_f32 v[96:97], v[32:33], v[46:47]
	v_pk_fma_f32 v[32:33], v[108:109], v[30:31], v[96:97] op_sel_hi:[0,1,1]
	v_pk_fma_f32 v[112:113], v[152:153], v[30:31], v[96:97] op_sel_hi:[0,1,1]
	v_pk_fma_f32 v[32:33], v[108:109], v[36:37], v[32:33] op_sel:[1,0,0]
	v_pk_fma_f32 v[112:113], v[152:153], v[36:37], v[112:113] op_sel:[1,0,0]
	v_pk_fma_f32 v[32:33], v[110:111], v[54:55], v[32:33] op_sel_hi:[0,1,1]
	v_pk_fma_f32 v[112:113], v[154:155], v[54:55], v[112:113] op_sel_hi:[0,1,1]
	v_pk_fma_f32 v[96:97], v[144:145], v[30:31], v[96:97] op_sel_hi:[0,1,1]
	v_pk_fma_f32 v[96:97], v[144:145], v[36:37], v[96:97] op_sel:[1,0,0]
	v_pk_fma_f32 v[96:97], v[146:147], v[54:55], v[96:97] op_sel_hi:[0,1,1]
	v_cndmask_b32_e64 v62, 0, v18, s[10:11]
	v_cndmask_b32_e64 v63, 0, v18, s[14:15]
	v_add_f32_dpp v96, v32, v96 wave_shl:1 row_mask:0xf bank_mask:0xf bound_ctrl:1
	v_add_f32_dpp v97, v33, v97 wave_shl:1 row_mask:0xf bank_mask:0xf bound_ctrl:1
	s_add_i32 s4, s34, 7
	s_cmpk_lt_i32 s4, 0x201
	s_cselect_b64 s[12:13], s[0:1], 0
	v_add_f32_dpp v96, v112, v96 wave_shr:1 row_mask:0xf bank_mask:0xf bound_ctrl:1
	v_add_f32_dpp v97, v113, v97 wave_shr:1 row_mask:0xf bank_mask:0xf bound_ctrl:1
	v_pk_fma_f32 v[96:97], v[34:35], v[106:107], v[96:97] op_sel_hi:[1,0,1] neg_lo:[0,0,1] neg_hi:[0,0,1]
	v_pk_add_f32 v[96:97], v[96:97], v[62:63] neg_lo:[0,1] neg_hi:[0,1]
	v_pk_mul_f32 v[70:71], v[96:97], v[96:97]
	v_add_f32_e32 v70, v70, v71
	v_cndmask_b32_e64 v71, 0, v70, s[12:13]
	v_add_f32_e32 v1, v1, v71
	s_waitcnt vmcnt(4)
	v_pk_add_f32 v[30:31], v[132:133], v[128:129]
	v_pk_mul_f32 v[32:33], v[132:133], v[132:133] op_sel_hi:[0,1]
	v_pk_mul_f32 v[34:35], v[132:133], v[134:135] op_sel_hi:[1,0]
	v_mul_f32_e64 v36, v133, v133
	v_mul_f32_e64 v37, v134, v134
	v_add_f32_e64 v54, v134, v130
	v_pk_add_f32 v[30:31], v[30:31], v[136:137]
	v_or3_b32 v17, v56, v59, v90
	v_or3_b32 v17, v17, v91, v57
	s_add_i32 s4, s34, 8
	s_cmpk_lt_u32 s4, 0x1ff
	s_cselect_b64 s[12:13], s[42:43], 0
	v_cmp_ne_u32_e64 s[30:31], 0, v17
	s_and_b64 s[30:31], s[30:31], s[12:13]
	v_cndmask_b32_e64 v17, 0, 1.0, s[30:31]
	v_pk_fma_f32 v[32:33], v[128:129], v[128:129], v[32:33] op_sel_hi:[0,1,1]
	v_pk_fma_f32 v[34:35], v[128:129], v[130:131], v[34:35] op_sel_hi:[1,0,1]
	v_fma_f32 v36, v129, v129, v36
	v_fma_f32 v37, v130, v130, v37
	v_add_f32_dpp v55, v17, v17 wave_shr:1 row_mask:0xf bank_mask:0xf bound_ctrl:1
	v_add_f32_e64 v54, v54, v138
	v_pk_fma_f32 v[32:33], v[136:137], v[136:137], v[32:33] op_sel_hi:[0,1,1]
	v_pk_fma_f32 v[34:35], v[136:137], v[138:139], v[34:35] op_sel_hi:[1,0,1]
	v_fma_f32 v36, v137, v137, v36
	v_fma_f32 v37, v138, v138, v37
	v_add_f32_dpp v55, v17, v55 wave_shl:1 row_mask:0xf bank_mask:0xf bound_ctrl:1
	v_pk_add_f32 v[84:85], v[4:5], v[30:31]
	v_pk_add_f32 v[62:63], v[6:7], v[84:85]
	v_pk_add_f32 v[4:5], v[8:9], v[32:33]
	v_pk_add_f32 v[6:7], v[10:11], v[4:5]
	v_pk_add_f32 v[10:11], v[14:15], v[34:35]
	v_pk_add_f32 v[8:9], v[72:73], v[10:11]
	v_pk_add_f32 v[14:15], v[20:21], v[36:37]
	v_pk_add_f32 v[70:71], v[88:89], v[14:15]
	v_pk_add_f32 v[86:87], v[52:53], v[54:55]
	v_pk_add_f32 v[20:21], v[92:93], v[86:87]
	v_mul_f32_e64 v92, v62, v22
	v_mul_f32_e64 v93, v63, v22
	v_mul_f32_e64 v94, v20, v22
	v_fma_f32 v17, v6, v22, v26
	v_mul_f32_e64 v29, v7, v22
	v_mul_f32_e64 v58, v8, v22
	v_fma_f32 v52, v70, v22, v26
	v_mul_f32_e64 v53, v9, v22
	v_fma_f32 v72, v71, v22, v26
	v_fma_f32 v17, -v92, v92, v17
	v_fma_f32 v29, -v92, v93, v29
	v_fma_f32 v58, -v92, v94, v58
	v_fma_f32 v52, -v93, v93, v52
	v_fma_f32 v53, -v93, v94, v53
	v_fma_f32 v72, -v94, v94, v72
	v_mul_f32_e64 v73, v53, v53
	v_mul_f32_e64 v88, v29, v72
	v_mul_f32_e64 v89, v58, v52
	v_mul_f32_e64 v104, v58, v58
	v_mul_f32_e64 v105, v17, v53
	v_mul_f32_e64 v106, v29, v29
	v_fma_f32 v73, v52, v72, -v73
	v_fma_f32 v88, v58, v53, -v88
	v_fma_f32 v89, v29, v53, -v89
	v_fma_f32 v104, v17, v72, -v104
	v_fma_f32 v105, v29, v58, -v105
	v_fma_f32 v106, v17, v52, -v106
	v_mul_f32_e64 v107, v17, v73
	v_fma_f32 v107, v29, v88, v107
	v_fma_f32 v107, v58, v89, v107
	v_rcp_f32_e32 v107, v107
	v_cmp_ne_u32_e64 vcc, s37, v25
	v_mul_f32_e64 v107, v107, v22
	v_cndmask_b32_e64 v107, 0, v107, s[30:31]
	v_cndmask_b32_e64 v17, 0, v18, vcc
	v_cndmask_b32_e64 v101, 0, v22, s[30:31]
	v_mul_f32_e64 v95, v73, v107
	v_mul_f32_e64 v96, v88, v107
	v_mul_f32_e64 v97, v89, v107
	v_mul_f32_e64 v98, v104, v107
	v_mul_f32_e64 v99, v105, v107
	v_mul_f32_e64 v100, v106, v107
	v_add_f32_e64 v102, v21, v17
	v_mov_b32_e32 v103, v25
	ds_write_b128 v23, v[92:95]
	ds_write_b128 v23, v[96:99] offset:1024
	ds_write_b128 v23, v[100:103] offset:2048
	v_mov_b32_dpp v6, v60 wave_shr:1 row_mask:0xf bank_mask:0xf bound_ctrl:1
	v_mov_b32_dpp v7, v61 wave_shr:1 row_mask:0xf bank_mask:0xf bound_ctrl:1
	v_mov_b32_dpp v62, v60 wave_shl:1 row_mask:0xf bank_mask:0xf bound_ctrl:1
	v_mov_b32_dpp v63, v61 wave_shl:1 row_mask:0xf bank_mask:0xf bound_ctrl:1
	v_pk_mul_f32 v[8:9], v[60:61], v[132:133] op_sel_hi:[1,0]
	v_pk_mul_f32 v[20:21], v[60:61], v[132:133] op_sel:[0,1]
	v_pk_mul_f32 v[52:53], v[60:61], v[134:135] op_sel_hi:[1,0]
	v_pk_add_f32 v[72:73], v[60:61], v[6:7]
	v_pk_fma_f32 v[8:9], v[6:7], v[128:129], v[8:9] op_sel_hi:[1,0,1]
	v_pk_fma_f32 v[20:21], v[6:7], v[128:129], v[20:21] op_sel:[0,1,0]
	v_pk_fma_f32 v[52:53], v[6:7], v[130:131], v[52:53] op_sel_hi:[1,0,1]
	v_pk_add_f32 v[72:73], v[72:73], v[62:63]
	v_pk_fma_f32 v[8:9], v[62:63], v[136:137], v[8:9] op_sel_hi:[1,0,1]
	v_pk_fma_f32 v[20:21], v[62:63], v[136:137], v[20:21] op_sel:[0,1,0]
	v_pk_fma_f32 v[52:53], v[62:63], v[138:139], v[52:53] op_sel_hi:[1,0,1]
	s_waitcnt lgkmcnt(0)
	s_barrier
	s_waitcnt vmcnt(0)
	s_add_i32 s4, s34, 12
	s_cmpk_lt_u32 s4, 0x201
	s_cselect_b64 s[12:13], s[40:41], 0
	v_cmp_eq_u32_e64 s[14:15], s37, v16
	s_and_b64 s[14:15], s[14:15], s[12:13]
	v_cndmask_b32_e64 v17, 0, 1, s[14:15]
	v_mov_b32_dpp v104, v172 wave_shr:1 row_mask:0xf bank_mask:0xf bound_ctrl:1
	v_mov_b32_dpp v105, v173 wave_shr:1 row_mask:0xf bank_mask:0xf bound_ctrl:1
	v_or_b32_dpp v25, v17, v17 wave_shr:1 row_mask:0xf bank_mask:0xf bound_ctrl:1
	v_mov_b32_dpp v106, v174 wave_shr:1 row_mask:0xf bank_mask:0xf bound_ctrl:1
	v_or_b32_dpp v25, v17, v25 wave_shl:1 row_mask:0xf bank_mask:0xf bound_ctrl:1
	v_mov_b32_dpp v108, v172 wave_shl:1 row_mask:0xf bank_mask:0xf bound_ctrl:1
	v_mov_b32_dpp v109, v173 wave_shl:1 row_mask:0xf bank_mask:0xf bound_ctrl:1
	v_or_b32_dpp v29, v25, v25 wave_shr:1 row_mask:0xf bank_mask:0xf bound_ctrl:1
	v_mov_b32_dpp v110, v174 wave_shl:1 row_mask:0xf bank_mask:0xf bound_ctrl:1
	v_or_b32_dpp v29, v25, v29 wave_shl:1 row_mask:0xf bank_mask:0xf bound_ctrl:1
	v_pk_add_f32 v[6:7], v[126:127], v[72:73]
	v_pk_add_f32 v[62:63], v[156:157], v[6:7]
	v_pk_add_f32 v[70:71], v[42:43], v[8:9]
	v_pk_add_f32 v[88:89], v[40:41], v[70:71]
	v_pk_add_f32 v[42:43], v[114:115], v[20:21]
	v_pk_add_f32 v[40:41], v[76:77], v[42:43]
	v_pk_add_f32 v[114:115], v[118:119], v[52:53]
	v_pk_add_f32 v[76:77], v[148:149], v[114:115]
	v_pk_fma_f32 v[88:89], v[92:93], v[62:63], v[88:89] op_sel_hi:[0,1,1] neg_lo:[1,0,0] neg_hi:[1,0,0]
	v_pk_fma_f32 v[40:41], v[92:93], v[62:63], v[40:41] op_sel:[1,0,0] neg_lo:[1,0,0] neg_hi:[1,0,0]
	v_pk_fma_f32 v[76:77], v[94:95], v[62:63], v[76:77] op_sel_hi:[0,1,1] neg_lo:[1,0,0] neg_hi:[1,0,0]
	v_pk_mul_f32 v[118:119], v[94:95], v[88:89] op_sel:[1,0]
	v_pk_mul_f32 v[126:127], v[96:97], v[88:89] op_sel_hi:[0,1]
	v_pk_mul_f32 v[146:147], v[96:97], v[88:89] op_sel:[1,0]
	v_pk_fma_f32 v[118:119], v[96:97], v[40:41], v[118:119] op_sel_hi:[0,1,1]
	v_pk_fma_f32 v[126:127], v[98:99], v[40:41], v[126:127] op_sel_hi:[0,1,1]
	v_pk_fma_f32 v[146:147], v[98:99], v[40:41], v[146:147] op_sel:[1,0,0]
	v_pk_fma_f32 v[118:119], v[96:97], v[76:77], v[118:119] op_sel:[1,0,0]
	v_pk_fma_f32 v[126:127], v[98:99], v[76:77], v[126:127] op_sel:[1,0,0]
	v_pk_fma_f32 v[146:147], v[100:101], v[76:77], v[146:147] op_sel_hi:[0,1,1]
	v_pk_mul_f32 v[112:113], v[92:93], v[118:119] op_sel_hi:[0,1]
	v_pk_fma_f32 v[112:113], v[92:93], v[126:127], v[112:113] op_sel:[1,0,0]
	v_pk_fma_f32 v[112:113], v[94:95], v[146:147], v[112:113] op_sel_hi:[0,1,1]
	v_pk_fma_f32 v[112:113], v[100:101], v[62:63], v[112:113] op_sel:[1,0,0] neg_lo:[0,0,1] neg_hi:[0,0,1]
	v_cmp_eq_u32_e64 s[10:11], 6, v103
	v_cmp_eq_u32_e64 s[14:15], 7, v103
	v_pk_add_f32 v[40:41], v[48:49], v[118:119]
	v_pk_add_f32 v[62:63], v[74:75], v[40:41]
	v_pk_add_f32 v[48:49], v[68:69], v[126:127]
	v_pk_add_f32 v[74:75], v[78:79], v[48:49]
	v_pk_add_f32 v[68:69], v[80:81], v[146:147]
	v_pk_add_f32 v[76:77], v[82:83], v[68:69]
	v_pk_add_f32 v[78:79], v[46:47], v[112:113]
	v_pk_add_f32 v[80:81], v[44:45], v[78:79]
	v_pk_fma_f32 v[44:45], v[140:141], v[62:63], v[80:81] op_sel_hi:[0,1,1]
	v_pk_fma_f32 v[88:89], v[168:169], v[62:63], v[80:81] op_sel_hi:[0,1,1]
	v_pk_fma_f32 v[44:45], v[140:141], v[74:75], v[44:45] op_sel:[1,0,0]
	v_pk_fma_f32 v[88:89], v[168:169], v[74:75], v[88:89] op_sel:[1,0,0]
	v_pk_fma_f32 v[44:45], v[142:143], v[76:77], v[44:45] op_sel_hi:[0,1,1]
	v_pk_fma_f32 v[88:89], v[170:171], v[76:77], v[88:89] op_sel_hi:[0,1,1]
	v_pk_fma_f32 v[80:81], v[120:121], v[62:63], v[80:81] op_sel_hi:[0,1,1]
	v_pk_fma_f32 v[80:81], v[120:121], v[74:75], v[80:81] op_sel:[1,0,0]
	v_pk_fma_f32 v[80:81], v[122:123], v[76:77], v[80:81] op_sel_hi:[0,1,1]
	v_cndmask_b32_e64 v46, 0, v18, s[10:11]
	v_cndmask_b32_e64 v47, 0, v18, s[14:15]
	v_add_f32_dpp v80, v44, v80 wave_shl:1 row_mask:0xf bank_mask:0xf bound_ctrl:1
	v_add_f32_dpp v81, v45, v81 wave_shl:1 row_mask:0xf bank_mask:0xf bound_ctrl:1
	s_add_i32 s4, s34, 8
	s_cmpk_lt_i32 s4, 0x201
	s_cselect_b64 s[12:13], s[0:1], 0
	v_add_f32_dpp v80, v88, v80 wave_shr:1 row_mask:0xf bank_mask:0xf bound_ctrl:1
	v_add_f32_dpp v81, v89, v81 wave_shr:1 row_mask:0xf bank_mask:0xf bound_ctrl:1
	v_pk_fma_f32 v[80:81], v[12:13], v[102:103], v[80:81] op_sel_hi:[1,0,1] neg_lo:[0,0,1] neg_hi:[0,0,1]
	v_pk_add_f32 v[80:81], v[80:81], v[46:47] neg_lo:[0,1] neg_hi:[0,1]
	v_pk_mul_f32 v[82:83], v[80:81], v[80:81]
	v_add_f32_e32 v82, v82, v83
	v_cndmask_b32_e64 v83, 0, v82, s[12:13]
	v_add_f32_e32 v1, v1, v83
	s_waitcnt vmcnt(0)
	v_pk_add_f32 v[12:13], v[172:173], v[104:105]
	v_pk_mul_f32 v[44:45], v[172:173], v[172:173] op_sel_hi:[0,1]
	v_pk_mul_f32 v[46:47], v[172:173], v[174:175] op_sel_hi:[1,0]
	v_mul_f32_e64 v62, v173, v173
	v_mul_f32_e64 v63, v174, v174
	v_add_f32_e64 v74, v174, v106
	v_pk_add_f32 v[12:13], v[12:13], v[108:109]
	v_or3_b32 v17, v29, v56, v59
	v_or3_b32 v17, v17, v90, v91
	s_add_i32 s4, s34, 9
	s_cmpk_lt_u32 s4, 0x1ff
	s_cselect_b64 s[12:13], s[42:43], 0
	v_cmp_ne_u32_e64 s[30:31], 0, v17
	s_and_b64 s[30:31], s[30:31], s[12:13]
	v_cndmask_b32_e64 v17, 0, 1.0, s[30:31]
	v_pk_fma_f32 v[44:45], v[104:105], v[104:105], v[44:45] op_sel_hi:[0,1,1]
	v_pk_fma_f32 v[46:47], v[104:105], v[106:107], v[46:47] op_sel_hi:[1,0,1]
	v_fma_f32 v62, v105, v105, v62
	v_fma_f32 v63, v106, v106, v63
	v_add_f32_dpp v75, v17, v17 wave_shr:1 row_mask:0xf bank_mask:0xf bound_ctrl:1
	v_add_f32_e64 v74, v74, v110
	v_pk_fma_f32 v[44:45], v[108:109], v[108:109], v[44:45] op_sel_hi:[0,1,1]
	v_pk_fma_f32 v[46:47], v[108:109], v[110:111], v[46:47] op_sel_hi:[1,0,1]
	v_fma_f32 v62, v109, v109, v62
	v_fma_f32 v63, v110, v110, v63
	v_add_f32_dpp v75, v17, v75 wave_shl:1 row_mask:0xf bank_mask:0xf bound_ctrl:1
	v_pk_add_f32 v[76:77], v[84:85], v[12:13]
	v_pk_add_f32 v[80:81], v[4:5], v[44:45]
	v_pk_add_f32 v[4:5], v[10:11], v[46:47]
	v_pk_add_f32 v[10:11], v[14:15], v[62:63]
	v_pk_add_f32 v[14:15], v[86:87], v[74:75]
	v_mul_f32_e64 v84, v76, v22
	v_mul_f32_e64 v85, v77, v22
	v_mul_f32_e64 v86, v14, v22
	v_fma_f32 v17, v80, v22, v26
	v_mul_f32_e64 v25, v81, v22
	v_mul_f32_e64 v57, v4, v22
	v_fma_f32 v58, v10, v22, v26
	v_mul_f32_e64 v82, v5, v22
	v_fma_f32 v83, v11, v22, v26
	v_fma_f32 v17, -v84, v84, v17
	v_fma_f32 v25, -v84, v85, v25
	v_fma_f32 v57, -v84, v86, v57
	v_fma_f32 v58, -v85, v85, v58
	v_fma_f32 v82, -v85, v86, v82
	v_fma_f32 v83, -v86, v86, v83
	v_mul_f32_e64 v88, v82, v82
	v_mul_f32_e64 v89, v25, v83
	v_mul_f32_e64 v100, v57, v58
	v_mul_f32_e64 v101, v57, v57
	v_mul_f32_e64 v102, v17, v82
	v_mul_f32_e64 v103, v25, v25
	v_fma_f32 v88, v58, v83, -v88
	v_fma_f32 v89, v57, v82, -v89
	v_fma_f32 v100, v25, v82, -v100
	v_fma_f32 v101, v17, v83, -v101
	v_fma_f32 v102, v25, v57, -v102
	v_fma_f32 v103, v17, v58, -v103
	v_mul_f32_e64 v116, v17, v88
	v_fma_f32 v116, v25, v89, v116
	v_fma_f32 v116, v57, v100, v116
	v_rcp_f32_e32 v116, v116
	v_cmp_ne_u32_e64 vcc, s37, v24
	v_mul_f32_e64 v116, v116, v22
	v_cndmask_b32_e64 v116, 0, v116, s[30:31]
	v_cndmask_b32_e64 v17, 0, v18, vcc
	v_cndmask_b32_e64 v97, 0, v22, s[30:31]
	v_mul_f32_e64 v87, v88, v116
	v_mul_f32_e64 v92, v89, v116
	v_mul_f32_e64 v93, v100, v116
	v_mul_f32_e64 v94, v101, v116
	v_mul_f32_e64 v95, v102, v116
	v_mul_f32_e64 v96, v103, v116
	v_add_f32_e64 v98, v15, v17
	v_mov_b32_e32 v99, v24
	ds_write_b128 v23, v[84:87] offset:3072
	ds_write_b128 v23, v[92:95] offset:4096
	ds_write_b128 v23, v[96:99] offset:5120
	v_mov_b32_dpp v4, v38 wave_shr:1 row_mask:0xf bank_mask:0xf bound_ctrl:1
	v_mov_b32_dpp v5, v39 wave_shr:1 row_mask:0xf bank_mask:0xf bound_ctrl:1
	v_mov_b32_dpp v24, v38 wave_shl:1 row_mask:0xf bank_mask:0xf bound_ctrl:1
	v_mov_b32_dpp v25, v39 wave_shl:1 row_mask:0xf bank_mask:0xf bound_ctrl:1
	v_pk_mul_f32 v[10:11], v[38:39], v[172:173] op_sel_hi:[1,0]
	v_pk_mul_f32 v[14:15], v[38:39], v[172:173] op_sel:[0,1]
	v_pk_mul_f32 v[82:83], v[38:39], v[174:175] op_sel_hi:[1,0]
	v_pk_add_f32 v[102:103], v[38:39], v[4:5]
	v_pk_fma_f32 v[10:11], v[4:5], v[104:105], v[10:11] op_sel_hi:[1,0,1]
	v_pk_fma_f32 v[14:15], v[4:5], v[104:105], v[14:15] op_sel:[0,1,0]
	v_pk_fma_f32 v[82:83], v[4:5], v[106:107], v[82:83] op_sel_hi:[1,0,1]
	v_pk_add_f32 v[102:103], v[102:103], v[24:25]
	v_pk_fma_f32 v[10:11], v[24:25], v[108:109], v[10:11] op_sel_hi:[1,0,1]
	v_pk_fma_f32 v[14:15], v[24:25], v[108:109], v[14:15] op_sel:[0,1,0]
	v_pk_fma_f32 v[82:83], v[24:25], v[110:111], v[82:83] op_sel_hi:[1,0,1]
	s_waitcnt lgkmcnt(0)
	s_barrier
	v_pk_add_f32 v[4:5], v[6:7], v[102:103]
	v_pk_add_f32 v[6:7], v[70:71], v[10:11]
	v_pk_add_f32 v[70:71], v[42:43], v[14:15]
	v_pk_add_f32 v[42:43], v[114:115], v[82:83]
	v_pk_fma_f32 v[6:7], v[84:85], v[4:5], v[6:7] op_sel_hi:[0,1,1] neg_lo:[1,0,0] neg_hi:[1,0,0]
	v_pk_fma_f32 v[70:71], v[84:85], v[4:5], v[70:71] op_sel:[1,0,0] neg_lo:[1,0,0] neg_hi:[1,0,0]
	v_pk_fma_f32 v[42:43], v[86:87], v[4:5], v[42:43] op_sel_hi:[0,1,1] neg_lo:[1,0,0] neg_hi:[1,0,0]
	v_pk_mul_f32 v[24:25], v[86:87], v[6:7] op_sel:[1,0]
	v_pk_mul_f32 v[76:77], v[92:93], v[6:7] op_sel_hi:[0,1]
	v_pk_mul_f32 v[80:81], v[92:93], v[6:7] op_sel:[1,0]
	v_pk_fma_f32 v[24:25], v[92:93], v[70:71], v[24:25] op_sel_hi:[0,1,1]
	v_pk_fma_f32 v[76:77], v[94:95], v[70:71], v[76:77] op_sel_hi:[0,1,1]
	v_pk_fma_f32 v[80:81], v[94:95], v[70:71], v[80:81] op_sel:[1,0,0]
	v_pk_fma_f32 v[24:25], v[92:93], v[42:43], v[24:25] op_sel:[1,0,0]
	v_pk_fma_f32 v[76:77], v[94:95], v[42:43], v[76:77] op_sel:[1,0,0]
	v_pk_fma_f32 v[80:81], v[96:97], v[42:43], v[80:81] op_sel_hi:[0,1,1]
	v_pk_mul_f32 v[114:115], v[84:85], v[24:25] op_sel_hi:[0,1]
	v_pk_fma_f32 v[114:115], v[84:85], v[76:77], v[114:115] op_sel:[1,0,0]
	v_pk_fma_f32 v[114:115], v[86:87], v[80:81], v[114:115] op_sel_hi:[0,1,1]
	v_pk_fma_f32 v[114:115], v[96:97], v[4:5], v[114:115] op_sel:[1,0,0] neg_lo:[0,0,1] neg_hi:[0,0,1]
	v_cmp_eq_u32_e64 s[10:11], 6, v99
	v_cmp_eq_u32_e64 s[14:15], 7, v99
	v_pk_add_f32 v[4:5], v[40:41], v[24:25]
	v_pk_add_f32 v[6:7], v[48:49], v[76:77]
	v_pk_add_f32 v[40:41], v[68:69], v[80:81]
	v_pk_add_f32 v[42:43], v[78:79], v[114:115]
	v_pk_fma_f32 v[70:71], v[176:177], v[4:5], v[42:43] op_sel_hi:[0,1,1]
	v_pk_fma_f32 v[78:79], v[180:181], v[4:5], v[42:43] op_sel_hi:[0,1,1]
	v_pk_fma_f32 v[70:71], v[176:177], v[6:7], v[70:71] op_sel:[1,0,0]
	v_pk_fma_f32 v[78:79], v[180:181], v[6:7], v[78:79] op_sel:[1,0,0]
	v_pk_fma_f32 v[70:71], v[178:179], v[40:41], v[70:71] op_sel_hi:[0,1,1]
	v_pk_fma_f32 v[78:79], v[182:183], v[40:41], v[78:79] op_sel_hi:[0,1,1]
	v_pk_fma_f32 v[42:43], v[64:65], v[4:5], v[42:43] op_sel_hi:[0,1,1]
	v_pk_fma_f32 v[42:43], v[64:65], v[6:7], v[42:43] op_sel:[1,0,0]
	v_pk_fma_f32 v[42:43], v[66:67], v[40:41], v[42:43] op_sel_hi:[0,1,1]
	v_cndmask_b32_e64 v48, 0, v18, s[10:11]
	v_cndmask_b32_e64 v49, 0, v18, s[14:15]
	v_add_f32_dpp v42, v70, v42 wave_shl:1 row_mask:0xf bank_mask:0xf bound_ctrl:1
	v_add_f32_dpp v43, v71, v43 wave_shl:1 row_mask:0xf bank_mask:0xf bound_ctrl:1
	s_add_i32 s4, s34, 9
	s_cmpk_lt_i32 s4, 0x201
	s_cselect_b64 s[12:13], s[0:1], 0
	v_add_f32_dpp v42, v78, v42 wave_shr:1 row_mask:0xf bank_mask:0xf bound_ctrl:1
	v_add_f32_dpp v43, v79, v43 wave_shr:1 row_mask:0xf bank_mask:0xf bound_ctrl:1
	v_pk_fma_f32 v[42:43], v[50:51], v[98:99], v[42:43] op_sel_hi:[1,0,1] neg_lo:[0,0,1] neg_hi:[0,0,1]
	v_pk_add_f32 v[42:43], v[42:43], v[48:49] neg_lo:[0,1] neg_hi:[0,1]
	v_pk_mul_f32 v[68:69], v[42:43], v[42:43]
	v_add_f32_e32 v68, v68, v69
	v_cndmask_b32_e64 v69, 0, v68, s[12:13]
	v_add_f32_e32 v1, v1, v69
	v_mov_b32_e32 v0, v1
	s_branch .LBB0_29
